# scan: 6-instruction bf16 RNE pack replaced by v_cvt_pk_bf16_f32 (63 sites) on top of v46
# speedup vs baseline: 1.0023x; 1.0004x over previous
.LBB0_467:
	s_and_b64 s[14:15], s[6:7], exec
	s_cselect_b32 s14, 0, 0x4400000
	s_add_u32 s14, s74, s14
	s_addc_u32 s15, s75, 0
	s_lshl_b32 s16, s33, 1
	s_add_u32 s14, s14, s16
	s_addc_u32 s15, s15, 0
	s_lshl_b32 s16, s54, 5
	s_or_b32 s33, s16, 6
	s_lshl_b32 s16, s83, 10
	s_add_u32 s66, s14, s16
	s_addc_u32 s67, s15, 0
	s_and_b32 s14, s82, 7
	s_lshl_b32 s15, s14, 6
	v_add_u32_e32 v213, s15, v185
	ds_read_b128 v[2:5], v213
	ds_read_b128 v[6:9], v213 offset:8448
	ds_read_b128 v[10:13], v213 offset:16896
	ds_read_b128 v[14:17], v213 offset:25344
	s_and_b32 s15, s55, 7
	s_lshl_b32 s16, s15, 6
	v_add_u32_e32 v214, s16, v185
	s_waitcnt vmcnt(17) lgkmcnt(3)
	v_mfma_f32_16x16x32_bf16 v[2:5], v[2:5], v[118:121], 0
	ds_read_b128 v[46:49], v214
	s_and_b32 s16, s56, 7
	s_lshl_b32 s17, s16, 6
	s_waitcnt lgkmcnt(3)
	v_mfma_f32_16x16x32_bf16 v[6:9], v[6:9], v[118:121], 0
	v_add_u32_e32 v215, s17, v185
	s_and_b32 s28, s57, 7
	s_lshl_b32 s17, s28, 6
	s_waitcnt lgkmcnt(2)
	v_mfma_f32_16x16x32_bf16 v[10:13], v[10:13], v[118:121], 0
	v_add_u32_e32 v216, s17, v185
	s_and_b32 s29, s60, 7
	s_lshl_b32 s17, s29, 6
	s_waitcnt lgkmcnt(1)
	v_mfma_f32_16x16x32_bf16 v[14:17], v[14:17], v[118:121], 0
	ds_read_b128 v[118:121], v214 offset:8448
	v_add_u32_e32 v217, s17, v185
	v_fmac_f32_e32 v135, v128, v129
	s_waitcnt vmcnt(16) lgkmcnt(1)
	v_mfma_f32_16x16x32_bf16 v[2:5], v[46:49], v[114:117], v[2:5]
	s_and_b32 s54, s63, 7
	s_lshl_b32 s40, s14, 10
	s_lshl_b32 s14, s54, 6
	s_waitcnt lgkmcnt(0)
	v_mfma_f32_16x16x32_bf16 v[6:9], v[118:121], v[114:117], v[6:9]
	ds_read_b128 v[46:49], v214 offset:16896
	ds_read_b128 v[118:121], v214 offset:25344
	v_add_u32_e32 v218, s14, v185
	s_and_b32 s56, s62, 7
	s_waitcnt lgkmcnt(1)
	v_mfma_f32_16x16x32_bf16 v[10:13], v[46:49], v[114:117], v[10:13]
	ds_read_b128 v[46:49], v215
	s_lshl_b32 s17, s56, 6
	v_add_u32_e32 v219, s17, v185
	s_waitcnt lgkmcnt(1)
	v_mfma_f32_16x16x32_bf16 v[14:17], v[118:121], v[114:117], v[14:17]
	ds_read_b128 v[114:117], v215 offset:8448
	v_exp_f32_e32 v118, v135
	s_lshl_b64 s[60:61], s[50:51], 16
	s_waitcnt vmcnt(15) lgkmcnt(1)
	v_mfma_f32_16x16x32_bf16 v[2:5], v[46:49], v[110:113], v[2:5]
	v_ldexp_f32 v158, v118, v126
	s_lshl_b32 s50, s28, 10
	s_and_b32 s28, s58, 7
	s_waitcnt lgkmcnt(0)
	v_mfma_f32_16x16x32_bf16 v[6:9], v[114:117], v[110:113], v[6:9]
	ds_read_b128 v[46:49], v215 offset:16896
	ds_read_b128 v[114:117], v215 offset:25344
	s_lshl_b32 s52, s28, 6
	v_add_u32_e32 v220, s52, v185
	s_waitcnt lgkmcnt(1)
	v_mfma_f32_16x16x32_bf16 v[10:13], v[46:49], v[110:113], v[10:13]
	ds_read_b128 v[46:49], v216
	v_mov_b32_e32 v159, v158
	s_lshl_b32 s16, s16, 10
	s_waitcnt lgkmcnt(1)
	v_mfma_f32_16x16x32_bf16 v[14:17], v[114:117], v[110:113], v[14:17]
	ds_read_b128 v[110:113], v216 offset:8448
	v_add_f32_e32 v114, v130, v134
	v_exp_f32_e32 v119, v114
	s_waitcnt vmcnt(14) lgkmcnt(1)
	v_mfma_f32_16x16x32_bf16 v[2:5], v[46:49], v[62:65], v[2:5]
	ds_read_b128 v[46:49], v216 offset:16896
	ds_read_b128 v[114:117], v217
	v_ldexp_f32 v160, v119, v127
	s_waitcnt lgkmcnt(2)
	v_mfma_f32_16x16x32_bf16 v[6:9], v[110:113], v[62:65], v[6:9]
	ds_read_b128 v[110:113], v216 offset:25344
	ds_read_b128 v[118:121], v218 offset:8448
	ds_read_b128 v[126:129], v220 offset:8448
	s_waitcnt lgkmcnt(4)
	v_mfma_f32_16x16x32_bf16 v[10:13], v[46:49], v[62:65], v[10:13]
	ds_read_b128 v[46:49], v217 offset:8448
	v_mov_b32_e32 v161, v160
	v_lshl_add_u64 v[134:135], v[150:151], 0, s[60:61]
	s_waitcnt lgkmcnt(3)
	v_mfma_f32_16x16x32_bf16 v[62:65], v[110:113], v[62:65], v[14:17]
	ds_read_b128 v[110:113], v218
	s_mov_b32 s17, s41
	s_lshl_b32 s52, s29, 10
	ds_read_b128 v[14:17], v217 offset:16896
	s_waitcnt vmcnt(13) lgkmcnt(2)
	v_mfma_f32_16x16x32_bf16 v[6:9], v[46:49], v[58:61], v[6:9]
	ds_read_b128 v[46:49], v217 offset:25344
	s_mov_b32 s53, s41
	s_lshl_b32 s54, s54, 10
	v_mfma_f32_16x16x32_bf16 v[2:5], v[114:117], v[58:61], v[2:5]
	s_mov_b32 s55, s41
	s_lshl_b32 s58, s28, 10
	s_mov_b32 s59, s41
	s_waitcnt lgkmcnt(1)
	v_mfma_f32_16x16x32_bf16 v[114:117], v[14:17], v[58:61], v[10:13]
	s_lshl_b32 s56, s56, 10
	s_mov_b32 s57, s41
	s_lshl_b32 s14, s15, 10
	s_waitcnt lgkmcnt(0)
	v_mfma_f32_16x16x32_bf16 v[46:49], v[46:49], v[58:61], v[62:65]
	ds_read_b128 v[58:61], v218 offset:16896
	v_lshl_add_u64 v[10:11], v[134:135], 0, s[40:41]
	s_mov_b32 s15, s41
	s_waitcnt vmcnt(12)
	v_mfma_f32_16x16x32_bf16 v[2:5], v[110:113], v[50:53], v[2:5]
	ds_read_b128 v[62:65], v218 offset:25344
	ds_read_b128 v[110:113], v219
	s_mov_b32 s51, s41
	v_mfma_f32_16x16x32_bf16 v[6:9], v[118:121], v[50:53], v[6:9]
	ds_read_b128 v[118:121], v219 offset:8448
	global_load_dwordx4 v[14:17], v[10:11], off
	s_add_u32 s28, s18, s60
	s_waitcnt lgkmcnt(2)
	v_mfma_f32_16x16x32_bf16 v[46:49], v[62:65], v[50:53], v[46:49]
	ds_read_b128 v[62:65], v219 offset:16896
	s_addc_u32 s29, s19, s61
	v_lshl_add_u64 v[138:139], s[28:29], 0, v[144:145]
	s_waitcnt vmcnt(12) lgkmcnt(2)
	v_mfma_f32_16x16x32_bf16 v[2:5], v[110:113], v[54:57], v[2:5]
	ds_read_b128 v[110:113], v219 offset:25344
	v_lshl_add_u64 v[140:141], v[138:139], 0, s[42:43]
	s_lshl_b32 s60, s37, 10
	s_waitcnt lgkmcnt(2)
	v_mfma_f32_16x16x32_bf16 v[6:9], v[118:121], v[54:57], v[6:9]
	ds_read_b128 v[118:121], v220
	s_mov_b32 s61, s41
	s_lshl_b32 s62, s49, 10
	s_waitcnt lgkmcnt(1)
	v_mfma_f32_16x16x32_bf16 v[46:49], v[110:113], v[54:57], v[46:49]
	ds_read_b128 v[110:113], v220 offset:16896
	s_mov_b32 s63, s41
	s_lshl_b32 s64, s64, 10
	s_waitcnt vmcnt(11) lgkmcnt(1)
	v_mfma_f32_16x16x32_bf16 v[118:121], v[118:121], v[106:109], v[2:5]
	s_mov_b32 s65, s41
	v_add_u32_e32 v221, 0x2000, v194
	v_add_u32_e32 v222, 0x4000, v194
	ds_read_b128 v[2:5], v220 offset:25344
	v_mfma_f32_16x16x32_bf16 v[114:117], v[58:61], v[50:53], v[114:117]
	v_lshl_add_u64 v[58:59], v[134:135], 0, s[16:17]
	global_load_dwordx4 v[58:61], v[58:59], off
	v_lshl_add_u64 v[50:51], v[134:135], 0, s[50:51]
	v_mfma_f32_16x16x32_bf16 v[114:117], v[62:65], v[54:57], v[114:117]
	v_lshl_add_u64 v[54:55], v[134:135], 0, s[52:53]
	global_load_dwordx4 v[62:65], v[54:55], off
	v_add_u32_e32 v223, 0x6000, v194
	v_mfma_f32_16x16x32_bf16 v[126:129], v[126:129], v[106:109], v[6:9]
	global_load_dwordx4 v[50:53], v[50:51], off
	v_lshl_add_u64 v[168:169], s[66:67], 0, v[142:143]
	v_mov_b32_e32 v162, v154
	s_waitcnt lgkmcnt(1)
	v_mfma_f32_16x16x32_bf16 v[110:113], v[110:113], v[106:109], v[114:117]
	v_lshl_add_u64 v[6:7], v[134:135], 0, s[54:55]
	global_load_dwordx4 v[54:57], v[6:7], off
	v_mov_b32_e32 v163, v154
	s_waitcnt lgkmcnt(0)
	v_mfma_f32_16x16x32_bf16 v[46:49], v[2:5], v[106:109], v[46:49]
	v_mul_f32_e64 v108, v158, v118
	v_mul_f32_e64 v109, v158, v119
	v_pk_mul_f32 v[106:107], v[158:159], v[120:121] op_sel_hi:[0,1]
	v_pk_fma_f32 v[18:19], v[160:161], v[18:19], v[108:109] op_sel_hi:[0,1,1]
	v_pk_fma_f32 v[20:21], v[160:161], v[20:21], v[106:107] op_sel_hi:[0,1,1]
	v_bfe_u32 v106, v18, 16, 1
	v_add3_u32 v18, v18, v106, s80
	v_bfe_u32 v106, v19, 16, 1
	v_lshrrev_b32_e32 v18, 16, v18
	v_add3_u32 v19, v19, v106, s80
	v_and_or_b32 v18, v19, s79, v18
	v_bfe_u32 v19, v20, 16, 1
	v_add3_u32 v19, v20, v19, s80
	v_bfe_u32 v20, v21, 16, 1
	v_lshrrev_b32_e32 v19, 16, v19
	v_add3_u32 v20, v21, v20, s80
	v_pk_mul_f32 v[106:107], v[158:159], v[126:127] op_sel_hi:[0,1]
	v_and_or_b32 v19, v20, s79, v19
	v_pk_mul_f32 v[20:21], v[158:159], v[128:129] op_sel_hi:[0,1]
	v_pk_fma_f32 v[22:23], v[160:161], v[22:23], v[106:107] op_sel_hi:[0,1,1]
	v_pk_fma_f32 v[20:21], v[160:161], v[24:25], v[20:21] op_sel_hi:[0,1,1]
	v_bfe_u32 v24, v22, 16, 1
	v_add3_u32 v22, v22, v24, s80
	v_bfe_u32 v24, v23, 16, 1
	v_lshrrev_b32_e32 v22, 16, v22
	v_add3_u32 v23, v23, v24, s80
	v_and_or_b32 v22, v23, s79, v22
	v_bfe_u32 v23, v20, 16, 1
	v_add3_u32 v20, v20, v23, s80
	v_bfe_u32 v23, v21, 16, 1
	v_lshrrev_b32_e32 v20, 16, v20
	v_add3_u32 v21, v21, v23, s80
	v_and_or_b32 v23, v21, s79, v20
	v_pk_mul_f32 v[20:21], v[158:159], v[110:111] op_sel_hi:[0,1]
	v_pk_fma_f32 v[20:21], v[160:161], v[26:27], v[20:21] op_sel_hi:[0,1,1]
	ds_write2_b64 v193, v[18:19], v[22:23] offset1:4
	v_bfe_u32 v22, v20, 16, 1
	v_pk_mul_f32 v[18:19], v[158:159], v[112:113] op_sel_hi:[0,1]
	v_add3_u32 v20, v20, v22, s80
	v_bfe_u32 v22, v21, 16, 1
	v_pk_fma_f32 v[18:19], v[160:161], v[28:29], v[18:19] op_sel_hi:[0,1,1]
	v_lshrrev_b32_e32 v20, 16, v20
	v_add3_u32 v21, v21, v22, s80
	v_and_or_b32 v20, v21, s79, v20
	v_bfe_u32 v21, v18, 16, 1
	v_pk_mul_f32 v[22:23], v[158:159], v[46:47] op_sel_hi:[0,1]
	v_add3_u32 v18, v18, v21, s80
	v_bfe_u32 v21, v19, 16, 1
	v_pk_fma_f32 v[22:23], v[160:161], v[30:31], v[22:23] op_sel_hi:[0,1,1]
	v_lshrrev_b32_e32 v18, 16, v18
	v_add3_u32 v19, v19, v21, s80
	v_bfe_u32 v24, v22, 16, 1
	v_and_or_b32 v21, v19, s79, v18
	v_pk_mul_f32 v[18:19], v[158:159], v[48:49] op_sel_hi:[0,1]
	v_add3_u32 v22, v22, v24, s80
	v_bfe_u32 v24, v23, 16, 1
	v_pk_fma_f32 v[18:19], v[160:161], v[32:33], v[18:19] op_sel_hi:[0,1,1]
	v_lshrrev_b32_e32 v22, 16, v22
	v_add3_u32 v23, v23, v24, s80
	v_and_or_b32 v22, v23, s79, v22
	v_bfe_u32 v23, v18, 16, 1
	v_lshl_add_u64 v[2:3], v[134:135], 0, s[58:59]
	v_add3_u32 v18, v18, v23, s80
	v_bfe_u32 v23, v19, 16, 1
	global_load_dwordx4 v[2:5], v[2:3], off
	v_lshl_add_u64 v[6:7], v[134:135], 0, s[56:57]
	v_lshrrev_b32_e32 v18, 16, v18
	v_add3_u32 v19, v19, v23, s80
	global_load_dwordx4 v[6:9], v[6:7], off
	v_lshl_add_u64 v[10:11], v[134:135], 0, s[14:15]
	v_and_or_b32 v23, v19, s79, v18
	global_load_dwordx4 v[10:13], v[10:11], off
	ds_write2_b64 v193, v[20:21], v[22:23] offset0:8 offset1:12
	s_waitcnt lgkmcnt(0)
	s_barrier
	ds_read_b64_tr_b16 v[24:25], v131 offset:34368
	ds_read_b64_tr_b16 v[22:23], v131 offset:33792
	ds_read_b64_tr_b16 v[26:27], v131 offset:33824
	ds_read_b64_tr_b16 v[30:31], v131 offset:33856
	ds_read_b64_tr_b16 v[46:47], v131 offset:33888
	ds_read_b64_tr_b16 v[28:29], v131 offset:34400
	ds_read_b64_tr_b16 v[32:33], v131 offset:34432
	ds_read_b64_tr_b16 v[48:49], v131 offset:34464
	v_mul_f32_e32 v18, 0, v154
	v_mov_b32_e32 v19, v18
	v_mov_b32_e32 v20, v18
	v_mov_b32_e32 v21, v18
	v_mov_b32_e32 v164, v160
	v_mov_b32_e32 v165, v160
	s_waitcnt vmcnt(17) lgkmcnt(6)
	v_mfma_f32_16x16x32_bf16 v[106:109], v[98:101], v[22:25], v[18:21]
	v_mov_b32_e32 v166, v158
	v_mov_b32_e32 v167, v158
	s_mov_b32 s37, 2
	s_waitcnt vmcnt(13)
	v_mfma_f32_16x16x32_bf16 v[22:25], v[102:105], v[22:25], v[18:21]
	s_mov_b32 s66, 34
	s_waitcnt lgkmcnt(2)
	v_mfma_f32_16x16x32_bf16 v[110:113], v[98:101], v[26:29], v[18:21]
	v_mfma_f32_16x16x32_bf16 v[26:29], v[102:105], v[26:29], v[18:21]
	s_waitcnt lgkmcnt(1)
	v_mfma_f32_16x16x32_bf16 v[114:117], v[98:101], v[30:33], v[18:21]
	v_mfma_f32_16x16x32_bf16 v[30:33], v[102:105], v[30:33], v[18:21]
	s_waitcnt lgkmcnt(0)
	v_mfma_f32_16x16x32_bf16 v[98:101], v[98:101], v[46:49], v[18:21]
	v_mfma_f32_16x16x32_bf16 v[18:21], v[102:105], v[46:49], v[18:21]
	ds_read_b64_tr_b16 v[48:49], v132 offset:34368
	ds_read_b64_tr_b16 v[46:47], v132 offset:33792
	ds_read_b64_tr_b16 v[102:103], v132 offset:33824
	ds_read_b64_tr_b16 v[118:119], v132 offset:33856
	ds_read_b64_tr_b16 v[126:127], v132 offset:33888
	ds_read_b64_tr_b16 v[104:105], v132 offset:34400
	ds_read_b64_tr_b16 v[120:121], v132 offset:34432
	ds_read_b64_tr_b16 v[128:129], v132 offset:34464
	s_waitcnt lgkmcnt(6)
	v_mfma_f32_16x16x32_bf16 v[106:109], v[90:93], v[46:49], v[106:109]
	s_waitcnt vmcnt(12)
	v_mfma_f32_16x16x32_bf16 v[22:25], v[94:97], v[46:49], v[22:25]
	s_waitcnt lgkmcnt(2)
	v_mfma_f32_16x16x32_bf16 v[46:49], v[90:93], v[102:105], v[110:113]
	v_mfma_f32_16x16x32_bf16 v[26:29], v[94:97], v[102:105], v[26:29]
	s_waitcnt lgkmcnt(1)
	v_mfma_f32_16x16x32_bf16 v[102:105], v[90:93], v[118:121], v[114:117]
	v_mfma_f32_16x16x32_bf16 v[30:33], v[94:97], v[118:121], v[30:33]
	s_waitcnt lgkmcnt(0)
	v_mfma_f32_16x16x32_bf16 v[90:93], v[90:93], v[126:129], v[98:101]
	v_mfma_f32_16x16x32_bf16 v[18:21], v[94:97], v[126:129], v[18:21]
	ds_read_b64_tr_b16 v[96:97], v133 offset:34368
	ds_read_b64_tr_b16 v[94:95], v133 offset:33792
	ds_read_b64_tr_b16 v[98:99], v133 offset:33824
	ds_read_b64_tr_b16 v[110:111], v133 offset:33856
	ds_read_b64_tr_b16 v[114:115], v133 offset:33888
	ds_read_b64_tr_b16 v[100:101], v133 offset:34400
	ds_read_b64_tr_b16 v[112:113], v133 offset:34432
	ds_read_b64_tr_b16 v[116:117], v133 offset:34464
	s_waitcnt lgkmcnt(6)
	v_mfma_f32_16x16x32_bf16 v[106:109], v[82:85], v[94:97], v[106:109]
	s_waitcnt vmcnt(11)
	v_mfma_f32_16x16x32_bf16 v[22:25], v[86:89], v[94:97], v[22:25]
	s_waitcnt lgkmcnt(0)
	v_mfma_f32_16x16x32_bf16 v[130:133], v[82:85], v[114:117], v[90:93]
	s_nop 2
	v_add_u32_e32 v90, s36, v178
	v_mfma_f32_16x16x32_bf16 v[46:49], v[82:85], v[98:101], v[46:49]
	v_mfma_f32_16x16x32_bf16 v[26:29], v[86:89], v[98:101], v[26:29]
	v_mfma_f32_16x16x32_bf16 v[126:129], v[82:85], v[110:113], v[102:105]
	v_mfma_f32_16x16x32_bf16 v[30:33], v[86:89], v[110:113], v[30:33]
	v_mfma_f32_16x16x32_bf16 v[18:21], v[86:89], v[114:117], v[18:21]
	ds_read_b64_tr_b16 v[84:85], v90 offset:34368
	ds_read_b64_tr_b16 v[82:83], v90 offset:33792
	ds_read_b64_tr_b16 v[86:87], v90 offset:33824
	ds_read_b64_tr_b16 v[114:115], v90 offset:33856
	ds_read_b64_tr_b16 v[134:135], v90 offset:33888
	ds_read_b64_tr_b16 v[88:89], v90 offset:34400
	ds_read_b64_tr_b16 v[116:117], v90 offset:34432
	ds_read_b64_tr_b16 v[136:137], v90 offset:34464
	s_waitcnt lgkmcnt(6)
	v_mfma_f32_16x16x32_bf16 v[118:121], v[74:77], v[82:85], v[106:109]
	s_waitcnt vmcnt(10)
	v_mfma_f32_16x16x32_bf16 v[98:101], v[78:81], v[82:85], v[22:25]
	s_nop 2
	v_lshl_add_u64 v[22:23], v[138:139], 0, s[60:61]
	v_lshl_add_u64 v[24:25], v[140:141], 0, s[60:61]
	global_load_dwordx4 v[94:97], v[22:23], off
	global_load_dwordx4 v[90:93], v[24:25], off
	v_lshl_add_u64 v[22:23], v[138:139], 0, s[62:63]
	v_lshl_add_u64 v[24:25], v[140:141], 0, s[62:63]
	s_waitcnt lgkmcnt(2)
	v_mfma_f32_16x16x32_bf16 v[102:105], v[74:77], v[86:89], v[46:49]
	v_mfma_f32_16x16x32_bf16 v[106:109], v[78:81], v[86:89], v[26:29]
	global_load_dwordx4 v[82:85], v[22:23], off
	global_load_dwordx4 v[86:89], v[24:25], off
	v_lshl_add_u64 v[22:23], v[138:139], 0, s[64:65]
	v_lshl_add_u64 v[24:25], v[140:141], 0, s[64:65]
	s_waitcnt lgkmcnt(1)
	v_mfma_f32_16x16x32_bf16 v[110:113], v[74:77], v[114:117], v[126:129]
	v_mfma_f32_16x16x32_bf16 v[114:117], v[78:81], v[114:117], v[30:33]
	global_load_dwordx4 v[26:29], v[22:23], off
	s_nop 1
	global_load_dwordx4 v[30:33], v[24:25], off
	s_waitcnt lgkmcnt(0)
	v_mfma_f32_16x16x32_bf16 v[78:81], v[78:81], v[134:137], v[18:21]
	v_cvt_pk_bf16_f32 v46, v118, v119
	v_lshl_add_u64 v[18:19], v[138:139], 0, s[46:47]
	v_lshl_add_u64 v[20:21], v[140:141], 0, s[46:47]
	global_load_dwordx4 v[22:25], v[18:19], off
	s_nop 0
	global_load_dwordx4 v[18:21], v[20:21], off
	v_cvt_pk_bf16_f32 v47, v120, v121
	v_cvt_pk_bf16_f32 v48, v102, v103
	v_cvt_pk_bf16_f32 v49, v104, v105
	v_mfma_f32_16x16x32_bf16 v[74:77], v[74:77], v[134:137], v[130:133]
	v_cvt_pk_bf16_f32 v126, v110, v111
	v_cvt_pk_bf16_f32 v127, v112, v113
	s_nop 5
	v_cvt_pk_bf16_f32 v128, v74, v75
	v_cvt_pk_bf16_f32 v129, v76, v77
	v_cvt_pk_bf16_f32 v130, v98, v99
	v_bfe_u32 v131, v100, 16, 1
	v_add3_u32 v131, v100, v131, s80
	v_bfe_u32 v132, v101, 16, 1
	v_lshrrev_b32_e32 v131, 16, v131
	v_add3_u32 v132, v101, v132, s80
	v_and_or_b32 v131, v132, s79, v131
	ds_write2_b64 v194, v[46:47], v[130:131] offset1:4
	v_cvt_pk_bf16_f32 v46, v106, v107
	v_cvt_pk_bf16_f32 v47, v108, v109
	ds_write2_b64 v221, v[48:49], v[46:47] offset0:32 offset1:36
	v_cvt_pk_bf16_f32 v46, v114, v115
	v_cvt_pk_bf16_f32 v47, v116, v117
	ds_write2_b64 v222, v[126:127], v[46:47] offset0:64 offset1:68
	v_cvt_pk_bf16_f32 v46, v78, v79
	v_cvt_pk_bf16_f32 v47, v80, v81
	ds_write2_b64 v223, v[128:129], v[46:47] offset0:96 offset1:100
	v_lshl_add_u32 v126, s48, 7, v179
	ds_read_b128 v[46:49], v184
	v_ashrrev_i32_e32 v127, 31, v126
	v_lshlrev_b64 v[126:127], 12, v[126:127]
	v_lshl_add_u64 v[130:131], v[168:169], 0, v[126:127]
	ds_read_b128 v[126:129], v184 offset:9216
	s_waitcnt lgkmcnt(1)
	global_store_dwordx4 v[130:131], v[46:49], off
	s_nop 1
	v_add_co_u32_e32 v46, vcc, s81, v130
	s_waitcnt vmcnt(18)
	v_and_b32_e32 v48, 0xffff0000, v71
	v_addc_co_u32_e32 v47, vcc, 0, v131, vcc
	s_waitcnt lgkmcnt(0)
	global_store_dwordx4 v[46:47], v[126:129], off
	v_lshlrev_b32_e32 v46, 16, v70
	v_and_b32_e32 v47, 0xffff0000, v70
	v_mul_f32_e32 v46, v195, v46
	v_mul_f32_e32 v47, v195, v47
	v_cvt_pk_bf16_f32 v46, v46, v47
	v_lshlrev_b32_e32 v47, 16, v71
	v_mul_f32_e32 v47, v195, v47
	v_mul_f32_e32 v48, v195, v48
	v_cvt_pk_bf16_f32 v47, v47, v48
	v_lshlrev_b32_e32 v48, 16, v72
	v_and_b32_e32 v49, 0xffff0000, v72
	v_mul_f32_e32 v48, v195, v48
	v_mul_f32_e32 v49, v195, v49
	v_cvt_pk_bf16_f32 v48, v48, v49
	v_lshlrev_b32_e32 v49, 16, v73
	v_mul_f32_e32 v49, v195, v49
	v_and_b32_e32 v70, 0xffff0000, v73
	v_mul_f32_e32 v70, v195, v70
	v_cvt_pk_bf16_f32 v49, v49, v70
	ds_write_b128 v183, v[46:49] offset:52224
	s_waitcnt vmcnt(18)
	v_lshlrev_b32_e32 v46, 16, v66
	v_and_b32_e32 v47, 0xffff0000, v66
	v_mul_f32_e32 v46, v196, v46
	v_mul_f32_e32 v47, v196, v47
	v_cvt_pk_bf16_f32 v46, v46, v47
	v_lshlrev_b32_e32 v47, 16, v67
	v_and_b32_e32 v48, 0xffff0000, v67
	v_mul_f32_e32 v47, v196, v47
	v_mul_f32_e32 v48, v196, v48
	v_cvt_pk_bf16_f32 v47, v47, v48
	v_lshlrev_b32_e32 v48, 16, v68
	v_and_b32_e32 v49, 0xffff0000, v68
	v_mul_f32_e32 v48, v196, v48
	v_mul_f32_e32 v49, v196, v49
	v_cvt_pk_bf16_f32 v48, v48, v49
	v_lshlrev_b32_e32 v49, 16, v69
	v_mul_f32_e32 v49, v196, v49
	v_and_b32_e32 v66, 0xffff0000, v69
	v_mul_f32_e32 v66, v196, v66
	v_cvt_pk_bf16_f32 v49, v49, v66
	ds_write_b128 v183, v[46:49] offset:61440
	v_mov_b64_e32 v[46:47], v[122:123]
	v_mov_b64_e32 v[48:49], v[124:125]
	s_waitcnt lgkmcnt(0)
	s_barrier
	s_branch .LBB0_469
.LBB0_468:
	ds_read_b128 v[226:229], v213
	ds_read_b128 v[234:237], v213 offset:8448
	ds_read_b128 v[238:241], v213 offset:16896
	ds_read_b128 v[242:245], v213 offset:25344
	ds_read_b128 v[246:249], v214
	s_waitcnt vmcnt(19) lgkmcnt(4)
	v_mfma_f32_16x16x32_bf16 v[226:229], v[226:229], v[14:17], 0
	s_cmp_lg_u32 s37, 2
	s_cselect_b32 s29, s66, 0
	s_and_b64 s[70:71], s[6:7], exec
	s_waitcnt lgkmcnt(3)
	v_mfma_f32_16x16x32_bf16 v[234:237], v[234:237], v[14:17], 0
	s_cselect_b32 s28, s28, s29
	s_or_b32 s29, s28, s84
	s_add_i32 s67, s28, s33
	s_waitcnt lgkmcnt(2)
	v_mfma_f32_16x16x32_bf16 v[238:241], v[238:241], v[14:17], 0
	s_cmp_lt_u32 s28, 2
	s_cselect_b32 s28, s29, s67
	s_lshl_b64 s[48:49], s[48:49], 16
	s_waitcnt lgkmcnt(1)
	v_mfma_f32_16x16x32_bf16 v[14:17], v[242:245], v[14:17], 0
	ds_read_b128 v[242:245], v214 offset:8448
	v_lshl_add_u64 v[140:141], v[150:151], 0, s[48:49]
	v_lshl_add_u64 v[172:173], v[140:141], 0, s[14:15]
	s_waitcnt vmcnt(12) lgkmcnt(1)
	v_mfma_f32_16x16x32_bf16 v[226:229], v[246:249], v[10:13], v[226:229]
	ds_read_b128 v[246:249], v214 offset:16896
	v_mov_b32_e32 v155, v154
	v_pk_mul_f32 v[120:121], v[154:155], v[120:121]
	s_waitcnt lgkmcnt(1)
	v_mfma_f32_16x16x32_bf16 v[234:237], v[242:245], v[10:13], v[234:237]
	ds_read_b128 v[242:245], v214 offset:25344
	v_pk_mul_f32 v[118:119], v[162:163], v[118:119]
	v_pk_mul_f32 v[100:101], v[154:155], v[100:101]
	s_waitcnt lgkmcnt(1)
	v_mfma_f32_16x16x32_bf16 v[238:241], v[246:249], v[10:13], v[238:241]
	ds_read_b128 v[246:249], v215
	v_pk_mul_f32 v[98:99], v[162:163], v[98:99]
	v_pk_mul_f32 v[104:105], v[154:155], v[104:105]
	s_waitcnt lgkmcnt(1)
	v_mfma_f32_16x16x32_bf16 v[10:13], v[242:245], v[10:13], v[14:17]
	ds_read_b128 v[242:245], v215 offset:16896
	s_nop 1
	ds_read_b128 v[14:17], v215 offset:8448
	v_pk_mul_f32 v[102:103], v[162:163], v[102:103]
	s_waitcnt lgkmcnt(0)
	v_mfma_f32_16x16x32_bf16 v[14:17], v[14:17], v[58:61], v[234:237]
	s_nop 2
	ds_read_b128 v[234:237], v215 offset:25344
	v_pk_mul_f32 v[108:109], v[154:155], v[108:109]
	v_pk_mul_f32 v[106:107], v[162:163], v[106:107]
	v_mfma_f32_16x16x32_bf16 v[226:229], v[246:249], v[58:61], v[226:229]
	v_mul_f32_e64 v112, v154, v112
	v_mul_f32_e64 v113, v155, v113
	v_pk_mul_f32 v[110:111], v[162:163], v[110:111]
	v_pk_mul_f32 v[116:117], v[154:155], v[116:117]
	v_mfma_f32_16x16x32_bf16 v[238:241], v[242:245], v[58:61], v[238:241]
	ds_read_b128 v[242:245], v216
	v_pk_mul_f32 v[114:115], v[162:163], v[114:115]
	v_pk_mul_f32 v[76:77], v[154:155], v[76:77]
	s_waitcnt lgkmcnt(1)
	v_mfma_f32_16x16x32_bf16 v[10:13], v[234:237], v[58:61], v[10:13]
	ds_read_b128 v[58:61], v216 offset:8448
	ds_read_b128 v[234:237], v216 offset:16896
	v_pk_mul_f32 v[74:75], v[162:163], v[74:75]
	s_waitcnt lgkmcnt(1)
	v_mfma_f32_16x16x32_bf16 v[14:17], v[58:61], v[50:53], v[14:17]
	ds_read_b128 v[58:61], v216 offset:25344
	v_pk_mul_f32 v[80:81], v[154:155], v[80:81]
	v_pk_mul_f32 v[78:79], v[162:163], v[78:79]
	v_mfma_f32_16x16x32_bf16 v[226:229], v[242:245], v[50:53], v[226:229]
	s_add_u32 s48, s18, s48
	s_addc_u32 s49, s19, s49
	s_bitcmp1_b32 s37, 0
	s_waitcnt lgkmcnt(1)
	v_mfma_f32_16x16x32_bf16 v[234:237], v[234:237], v[50:53], v[238:241]
	s_nop 2
	ds_read_b128 v[238:241], v217
	s_waitcnt lgkmcnt(1)
	v_mfma_f32_16x16x32_bf16 v[10:13], v[58:61], v[50:53], v[10:13]
	ds_read_b128 v[50:53], v217 offset:8448
	s_waitcnt lgkmcnt(1)
	v_mfma_f32_16x16x32_bf16 v[58:61], v[238:241], v[62:65], v[226:229]
	s_nop 2
	ds_read_b128 v[226:229], v217 offset:16896
	s_waitcnt lgkmcnt(1)
	v_mfma_f32_16x16x32_bf16 v[14:17], v[50:53], v[62:65], v[14:17]
	ds_read_b128 v[50:53], v217 offset:25344
	s_waitcnt lgkmcnt(1)
	v_mfma_f32_16x16x32_bf16 v[226:229], v[226:229], v[62:65], v[234:237]
	s_nop 2
	ds_read_b128 v[234:237], v218
	s_waitcnt lgkmcnt(1)
	v_mfma_f32_16x16x32_bf16 v[10:13], v[50:53], v[62:65], v[10:13]
	ds_read_b128 v[50:53], v218 offset:8448
	s_waitcnt lgkmcnt(1)
	v_mfma_f32_16x16x32_bf16 v[58:61], v[234:237], v[54:57], v[58:61]
	ds_read_b128 v[62:65], v218 offset:16896
	ds_read_b128 v[234:237], v218 offset:25344
	s_waitcnt lgkmcnt(2)
	v_mfma_f32_16x16x32_bf16 v[14:17], v[50:53], v[54:57], v[14:17]
	ds_read_b128 v[50:53], v219
	s_waitcnt lgkmcnt(2)
	v_mfma_f32_16x16x32_bf16 v[62:65], v[62:65], v[54:57], v[226:229]
	s_nop 2
	ds_read_b128 v[226:229], v219 offset:8448
	s_waitcnt lgkmcnt(2)
	v_mfma_f32_16x16x32_bf16 v[10:13], v[234:237], v[54:57], v[10:13]
	ds_read_b128 v[54:57], v219 offset:16896
	ds_read_b128 v[234:237], v220
	s_waitcnt lgkmcnt(3)
	v_mfma_f32_16x16x32_bf16 v[50:53], v[50:53], v[6:9], v[58:61]
	s_nop 2
	ds_read_b128 v[58:61], v219 offset:25344
	s_waitcnt lgkmcnt(3)
	v_mfma_f32_16x16x32_bf16 v[226:229], v[226:229], v[6:9], v[14:17]
	s_waitcnt lgkmcnt(2)
	v_mfma_f32_16x16x32_bf16 v[54:57], v[54:57], v[6:9], v[62:65]
	s_nop 0
	v_lshl_add_u64 v[14:15], v[140:141], 0, s[40:41]
	s_nop 0
	ds_read_b128 v[62:65], v220 offset:8448
	s_waitcnt lgkmcnt(1)
	v_mfma_f32_16x16x32_bf16 v[6:9], v[58:61], v[6:9], v[10:13]
	global_load_dwordx4 v[14:17], v[14:15], off
	s_nop 1
	global_load_dwordx4 v[10:13], v[172:173], off
	ds_read_b128 v[238:241], v220 offset:16896
	ds_read_b128 v[242:245], v220 offset:25344
	v_mfma_f32_16x16x32_bf16 v[234:237], v[234:237], v[2:5], v[50:53]
	v_lshl_add_u64 v[172:173], v[140:141], 0, s[54:55]
	s_nop 1
	v_lshl_add_u64 v[50:51], v[140:141], 0, s[16:17]
	v_lshl_add_u64 v[52:53], v[140:141], 0, s[50:51]
	s_waitcnt lgkmcnt(2)
	v_mfma_f32_16x16x32_bf16 v[226:229], v[62:65], v[2:5], v[226:229]
	v_lshl_add_u64 v[62:63], v[140:141], 0, s[52:53]
	global_load_dwordx4 v[58:61], v[50:51], off
	s_nop 0
	global_load_dwordx4 v[50:53], v[52:53], off
	s_waitcnt lgkmcnt(1)
	v_mfma_f32_16x16x32_bf16 v[238:241], v[238:241], v[2:5], v[54:57]
	global_load_dwordx4 v[62:65], v[62:63], off
	s_nop 1
	global_load_dwordx4 v[54:57], v[172:173], off
	v_lshl_add_u64 v[172:173], v[140:141], 0, s[56:57]
	v_lshl_add_u64 v[140:141], v[140:141], 0, s[58:59]
	s_waitcnt lgkmcnt(0)
	v_mfma_f32_16x16x32_bf16 v[242:245], v[242:245], v[2:5], v[6:9]
	s_nop 2
	global_load_dwordx4 v[6:9], v[172:173], off
	global_load_dwordx4 v[2:5], v[140:141], off
	v_pk_mul_f32 v[172:173], v[158:159], v[234:235]
	v_pk_mul_f32 v[140:141], v[166:167], v[236:237]
	v_pk_fma_f32 v[130:131], v[160:161], v[130:131], v[172:173]
	v_pk_fma_f32 v[132:133], v[164:165], v[132:133], v[140:141]
	v_bfe_u32 v140, v130, 16, 1
	v_add3_u32 v130, v130, v140, s80
	v_bfe_u32 v140, v131, 16, 1
	v_lshrrev_b32_e32 v130, 16, v130
	v_add3_u32 v131, v131, v140, s80
	v_and_or_b32 v130, v131, s79, v130
	v_bfe_u32 v131, v132, 16, 1
	v_add3_u32 v131, v132, v131, s80
	v_bfe_u32 v132, v133, 16, 1
	v_lshrrev_b32_e32 v131, 16, v131
	v_add3_u32 v132, v133, v132, s80
	v_pk_mul_f32 v[140:141], v[158:159], v[226:227]
	v_and_or_b32 v131, v132, s79, v131
	v_pk_mul_f32 v[132:133], v[166:167], v[228:229]
	v_pk_fma_f32 v[126:127], v[160:161], v[126:127], v[140:141]
	v_pk_fma_f32 v[128:129], v[164:165], v[128:129], v[132:133]
	v_bfe_u32 v132, v126, 16, 1
	v_add3_u32 v126, v126, v132, s80
	v_bfe_u32 v132, v127, 16, 1
	v_lshrrev_b32_e32 v126, 16, v126
	v_add3_u32 v127, v127, v132, s80
	v_and_or_b32 v126, v127, s79, v126
	v_bfe_u32 v127, v128, 16, 1
	v_add3_u32 v127, v128, v127, s80
	v_bfe_u32 v128, v129, 16, 1
	v_lshrrev_b32_e32 v127, 16, v127
	v_add3_u32 v128, v129, v128, s80
	v_and_or_b32 v127, v128, s79, v127
	v_pk_mul_f32 v[128:129], v[158:159], v[238:239]
	ds_write2_b64 v193, v[130:131], v[126:127] offset1:4
	v_pk_mul_f32 v[126:127], v[166:167], v[240:241]
	v_pk_fma_f32 v[122:123], v[160:161], v[122:123], v[128:129]
	v_pk_fma_f32 v[124:125], v[164:165], v[124:125], v[126:127]
	v_bfe_u32 v126, v122, 16, 1
	v_add3_u32 v122, v122, v126, s80
	v_bfe_u32 v126, v123, 16, 1
	v_lshrrev_b32_e32 v122, 16, v122
	v_add3_u32 v123, v123, v126, s80
	v_and_or_b32 v122, v123, s79, v122
	v_bfe_u32 v123, v124, 16, 1
	v_pk_mul_f32 v[126:127], v[158:159], v[242:243]
	v_add3_u32 v123, v124, v123, s80
	v_bfe_u32 v124, v125, 16, 1
	v_pk_fma_f32 v[126:127], v[160:161], v[134:135], v[126:127]
	v_lshrrev_b32_e32 v123, 16, v123
	v_add3_u32 v124, v125, v124, s80
	v_bfe_u32 v128, v126, 16, 1
	v_and_or_b32 v123, v124, s79, v123
	v_pk_mul_f32 v[124:125], v[166:167], v[244:245]
	v_add3_u32 v126, v126, v128, s80
	v_bfe_u32 v128, v127, 16, 1
	v_pk_fma_f32 v[124:125], v[164:165], v[136:137], v[124:125]
	v_lshrrev_b32_e32 v126, 16, v126
	v_add3_u32 v127, v127, v128, s80
	v_and_or_b32 v126, v127, s79, v126
	v_bfe_u32 v127, v124, 16, 1
	v_add3_u32 v124, v124, v127, s80
	v_bfe_u32 v127, v125, 16, 1
	v_lshrrev_b32_e32 v124, 16, v124
	v_add3_u32 v125, v125, v127, s80
	v_and_or_b32 v127, v125, s79, v124
	ds_write2_b64 v193, v[122:123], v[126:127] offset0:8 offset1:12
	s_waitcnt lgkmcnt(0)
	s_barrier
	ds_read_b64_tr_b16 v[124:125], v224 offset:34368
	ds_read_b64_tr_b16 v[122:123], v224 offset:33792
	ds_read_b64_tr_b16 v[126:127], v224 offset:33824
	ds_read_b64_tr_b16 v[130:131], v224 offset:33856
	ds_read_b64_tr_b16 v[134:135], v224 offset:33888
	ds_read_b64_tr_b16 v[128:129], v224 offset:34400
	ds_read_b64_tr_b16 v[132:133], v224 offset:34432
	ds_read_b64_tr_b16 v[136:137], v224 offset:34464
	s_waitcnt vmcnt(19) lgkmcnt(6)
	v_mfma_f32_16x16x32_bf16 v[118:121], v[94:97], v[122:125], v[118:121]
	s_waitcnt vmcnt(18)
	v_mfma_f32_16x16x32_bf16 v[98:101], v[90:93], v[122:125], v[98:101]
	s_waitcnt lgkmcnt(2)
	v_mfma_f32_16x16x32_bf16 v[102:105], v[94:97], v[126:129], v[102:105]
	v_mfma_f32_16x16x32_bf16 v[106:109], v[90:93], v[126:129], v[106:109]
	s_waitcnt lgkmcnt(1)
	v_mfma_f32_16x16x32_bf16 v[110:113], v[94:97], v[130:133], v[110:113]
	v_mfma_f32_16x16x32_bf16 v[114:117], v[90:93], v[130:133], v[114:117]
	v_lshl_add_u64 v[130:131], s[48:49], 0, v[144:145]
	v_lshl_add_u64 v[132:133], v[130:131], 0, s[42:43]
	s_waitcnt lgkmcnt(0)
	v_mfma_f32_16x16x32_bf16 v[74:77], v[94:97], v[134:137], v[74:77]
	v_mfma_f32_16x16x32_bf16 v[78:81], v[90:93], v[134:137], v[78:81]
	ds_read_b64_tr_b16 v[92:93], v225 offset:34368
	ds_read_b64_tr_b16 v[90:91], v225 offset:33792
	ds_read_b64_tr_b16 v[94:95], v225 offset:33824
	ds_read_b64_tr_b16 v[122:123], v225 offset:33856
	ds_read_b64_tr_b16 v[126:127], v225 offset:33888
	ds_read_b64_tr_b16 v[96:97], v225 offset:34400
	ds_read_b64_tr_b16 v[124:125], v225 offset:34432
	ds_read_b64_tr_b16 v[128:129], v225 offset:34464
	s_waitcnt vmcnt(17) lgkmcnt(6)
	v_mfma_f32_16x16x32_bf16 v[118:121], v[82:85], v[90:93], v[118:121]
	s_waitcnt vmcnt(16)
	v_mfma_f32_16x16x32_bf16 v[90:93], v[86:89], v[90:93], v[98:101]
	s_waitcnt lgkmcnt(2)
	v_mfma_f32_16x16x32_bf16 v[98:101], v[82:85], v[94:97], v[102:105]
	v_mfma_f32_16x16x32_bf16 v[94:97], v[86:89], v[94:97], v[106:109]
	s_waitcnt lgkmcnt(1)
	v_mfma_f32_16x16x32_bf16 v[102:105], v[82:85], v[122:125], v[110:113]
	v_mfma_f32_16x16x32_bf16 v[106:109], v[86:89], v[122:125], v[114:117]
	s_waitcnt lgkmcnt(0)
	v_mfma_f32_16x16x32_bf16 v[74:77], v[82:85], v[126:129], v[74:77]
	v_mfma_f32_16x16x32_bf16 v[78:81], v[86:89], v[126:129], v[78:81]
	ds_read_b64_tr_b16 v[84:85], v138 offset:34368
	ds_read_b64_tr_b16 v[82:83], v138 offset:33792
	ds_read_b64_tr_b16 v[86:87], v138 offset:33824
	ds_read_b64_tr_b16 v[110:111], v138 offset:33856
	ds_read_b64_tr_b16 v[114:115], v138 offset:33888
	ds_read_b64_tr_b16 v[88:89], v138 offset:34400
	ds_read_b64_tr_b16 v[112:113], v138 offset:34432
	ds_read_b64_tr_b16 v[116:117], v138 offset:34464
	s_waitcnt vmcnt(15) lgkmcnt(6)
	v_mfma_f32_16x16x32_bf16 v[118:121], v[26:29], v[82:85], v[118:121]
	s_waitcnt vmcnt(14)
	v_mfma_f32_16x16x32_bf16 v[82:85], v[30:33], v[82:85], v[90:93]
	s_waitcnt lgkmcnt(2)
	v_mfma_f32_16x16x32_bf16 v[90:93], v[26:29], v[86:89], v[98:101]
	v_mfma_f32_16x16x32_bf16 v[86:89], v[30:33], v[86:89], v[94:97]
	s_waitcnt lgkmcnt(1)
	v_mfma_f32_16x16x32_bf16 v[94:97], v[26:29], v[110:113], v[102:105]
	v_mfma_f32_16x16x32_bf16 v[122:125], v[30:33], v[110:113], v[106:109]
	s_waitcnt lgkmcnt(0)
	v_mfma_f32_16x16x32_bf16 v[26:29], v[26:29], v[114:117], v[74:77]
	v_mfma_f32_16x16x32_bf16 v[78:81], v[30:33], v[114:117], v[78:81]
	ds_read_b64_tr_b16 v[32:33], v139 offset:34368
	ds_read_b64_tr_b16 v[30:31], v139 offset:33792
	ds_read_b64_tr_b16 v[74:75], v139 offset:33824
	ds_read_b64_tr_b16 v[114:115], v139 offset:33856
	ds_read_b64_tr_b16 v[126:127], v139 offset:33888
	ds_read_b64_tr_b16 v[76:77], v139 offset:34400
	ds_read_b64_tr_b16 v[116:117], v139 offset:34432
	ds_read_b64_tr_b16 v[128:129], v139 offset:34464
	s_waitcnt vmcnt(13) lgkmcnt(6)
	v_mfma_f32_16x16x32_bf16 v[118:121], v[22:25], v[30:33], v[118:121]
	s_waitcnt vmcnt(12)
	v_mfma_f32_16x16x32_bf16 v[98:101], v[18:21], v[30:33], v[82:85]
	v_lshl_add_u64 v[30:31], v[130:131], 0, s[60:61]
	v_lshl_add_u64 v[32:33], v[132:133], 0, s[60:61]
	s_waitcnt lgkmcnt(2)
	v_mfma_f32_16x16x32_bf16 v[102:105], v[22:25], v[74:77], v[90:93]
	s_waitcnt lgkmcnt(1)
	v_mfma_f32_16x16x32_bf16 v[110:113], v[22:25], v[114:117], v[94:97]
	s_nop 2
	global_load_dwordx4 v[94:97], v[30:31], off
	global_load_dwordx4 v[90:93], v[32:33], off
	v_lshl_add_u64 v[30:31], v[130:131], 0, s[62:63]
	v_lshl_add_u64 v[32:33], v[132:133], 0, s[62:63]
	v_mfma_f32_16x16x32_bf16 v[106:109], v[18:21], v[74:77], v[86:89]
	global_load_dwordx4 v[82:85], v[30:31], off
	s_nop 1
	global_load_dwordx4 v[86:89], v[32:33], off
	v_lshl_add_u64 v[30:31], v[130:131], 0, s[64:65]
	v_mfma_f32_16x16x32_bf16 v[114:117], v[18:21], v[114:117], v[122:125]
	s_waitcnt lgkmcnt(0)
	v_mfma_f32_16x16x32_bf16 v[74:77], v[22:25], v[126:129], v[26:29]
	v_lshl_add_u64 v[22:23], v[132:133], 0, s[64:65]
	s_nop 1
	global_load_dwordx4 v[26:29], v[30:31], off
	s_nop 0
	global_load_dwordx4 v[30:33], v[22:23], off
	v_mfma_f32_16x16x32_bf16 v[78:81], v[18:21], v[126:129], v[78:81]
	v_lshl_add_u64 v[18:19], v[130:131], 0, s[46:47]
	v_lshl_add_u64 v[20:21], v[132:133], 0, s[46:47]
	global_load_dwordx4 v[22:25], v[18:19], off
	s_nop 0
	global_load_dwordx4 v[18:21], v[20:21], off
	v_cvt_pk_bf16_f32 v122, v118, v119
	v_cvt_pk_bf16_f32 v123, v120, v121
	v_cvt_pk_bf16_f32 v124, v102, v103
	v_cvt_pk_bf16_f32 v125, v104, v105
	v_cvt_pk_bf16_f32 v126, v110, v111
	v_cvt_pk_bf16_f32 v127, v112, v113
	v_cvt_pk_bf16_f32 v128, v74, v75
	v_cvt_pk_bf16_f32 v129, v76, v77
	v_cvt_pk_bf16_f32 v130, v98, v99
	v_cvt_pk_bf16_f32 v131, v100, v101
	ds_write2_b64 v194, v[122:123], v[130:131] offset1:4
	v_cvt_pk_bf16_f32 v122, v106, v107
	v_cvt_pk_bf16_f32 v123, v108, v109
	ds_write2_b64 v221, v[124:125], v[122:123] offset0:32 offset1:36
	v_cvt_pk_bf16_f32 v122, v114, v115
	v_cvt_pk_bf16_f32 v123, v116, v117
	ds_write2_b64 v222, v[126:127], v[122:123] offset0:64 offset1:68
	v_cvt_pk_bf16_f32 v122, v78, v79
	v_cvt_pk_bf16_f32 v123, v80, v81
	ds_write2_b64 v223, v[128:129], v[122:123] offset0:96 offset1:100
	v_lshl_add_u32 v126, s28, 7, v179
	ds_read_b128 v[122:125], v184
	v_ashrrev_i32_e32 v127, 31, v126
	v_lshlrev_b64 v[126:127], 12, v[126:127]
	v_lshl_add_u64 v[130:131], v[168:169], 0, v[126:127]
	ds_read_b128 v[126:129], v184 offset:9216
	s_waitcnt lgkmcnt(1)
	global_store_dwordx4 v[130:131], v[122:125], off
	s_cselect_b32 s28, 0x4800, 0
	s_add_i32 s37, s37, 1
	v_add_co_u32_e32 v122, vcc, s81, v130
	s_add_i32 s66, s66, -1
	s_nop 0
	v_addc_co_u32_e32 v123, vcc, 0, v131, vcc
	s_waitcnt lgkmcnt(0)
	global_store_dwordx4 v[122:123], v[126:129], off
	s_waitcnt vmcnt(19)
	v_lshlrev_b32_e32 v122, 16, v70
	v_and_b32_e32 v70, 0xffff0000, v70
	v_mul_f32_e32 v122, v195, v122
	v_mul_f32_e32 v70, v195, v70
	v_cvt_pk_bf16_f32 v70, v122, v70
	v_lshlrev_b32_e32 v122, 16, v71
	v_and_b32_e32 v71, 0xffff0000, v71
	v_mul_f32_e32 v122, v195, v122
	v_mul_f32_e32 v71, v195, v71
	v_cvt_pk_bf16_f32 v71, v122, v71
	v_lshlrev_b32_e32 v122, 16, v72
	v_and_b32_e32 v72, 0xffff0000, v72
	v_mul_f32_e32 v122, v195, v122
	v_mul_f32_e32 v72, v195, v72
	v_cvt_pk_bf16_f32 v72, v122, v72
	v_lshlrev_b32_e32 v122, 16, v73
	v_and_b32_e32 v73, 0xffff0000, v73
	v_mul_f32_e32 v122, v195, v122
	v_mul_f32_e32 v73, v195, v73
	v_cvt_pk_bf16_f32 v73, v122, v73
	v_add_u32_e32 v122, s28, v183
	ds_write_b128 v122, v[70:73] offset:33792
	s_waitcnt vmcnt(18)
	v_lshlrev_b32_e32 v70, 16, v66
	v_and_b32_e32 v66, 0xffff0000, v66
	v_mul_f32_e32 v70, v196, v70
	v_mul_f32_e32 v66, v196, v66
	v_cvt_pk_bf16_f32 v66, v70, v66
	v_lshlrev_b32_e32 v70, 16, v67
	v_and_b32_e32 v67, 0xffff0000, v67
	v_mul_f32_e32 v70, v196, v70
	v_mul_f32_e32 v67, v196, v67
	v_cvt_pk_bf16_f32 v67, v70, v67
	v_lshlrev_b32_e32 v70, 16, v68
	v_and_b32_e32 v68, 0xffff0000, v68
	v_mul_f32_e32 v70, v196, v70
	v_mul_f32_e32 v68, v196, v68
	v_cvt_pk_bf16_f32 v68, v70, v68
	v_lshlrev_b32_e32 v70, 16, v69
	v_and_b32_e32 v69, 0xffff0000, v69
	v_mul_f32_e32 v69, v196, v69
	s_cmp_eq_u32 s37, 35
	v_mul_f32_e32 v70, v196, v70
	v_cvt_pk_bf16_f32 v69, v70, v69
	ds_write_b128 v122, v[66:69] offset:43008
	s_waitcnt lgkmcnt(0)
	s_barrier
	s_cbranch_scc1 .LBB0_444

.LBB0_2522:
	s_and_b64 s[16:17], s[6:7], exec
	s_cselect_b32 s16, 0, 0x4400000
	s_add_u32 s16, s83, s16
	s_addc_u32 s17, s84, 0
	s_add_i32 s37, s88, 5
	s_add_i32 s36, s88, 6
	s_add_i32 s29, s88, -1
	s_lshl_b32 s44, s52, 1
	s_add_u32 s16, s16, s44
	s_addc_u32 s17, s17, 0
	s_lshl_b32 s44, s53, 5
	s_or_b32 s91, s44, 6
	s_lshl_b32 s44, s89, 10
	v_add_f32_e32 v18, v21, v25
	s_add_u32 s64, s16, s44
	v_fmac_f32_e32 v24, v1, v20
	v_exp_f32_e32 v18, v18
	s_addc_u32 s65, s17, 0
	s_lshl_b32 s16, s88, 5
	v_exp_f32_e32 v1, v24
	s_and_b32 s16, s16, 0x60
	v_add_u32_e32 v19, s16, v203
	v_cmp_le_i32_e32 vcc, v19, v65
	v_ldexp_f32 v190, v18, v23
	v_ldexp_f32 v188, v1, v22
	v_cndmask_b32_e64 v18, 0, 1, vcc
	v_cmp_ge_i32_e32 vcc, v19, v65
	v_or_b32_e32 v1, 1, v19
	s_lshl_b32 s16, s30, 5
	v_cndmask_b32_e64 v20, 0, 1, vcc
	v_cmp_lt_i32_e32 vcc, v19, v65
	v_cndmask_b32_e64 v18, v20, v18, s[6:7]
	v_and_b32_e32 v18, 1, v18
	v_cndmask_b32_e64 v20, 0, 1, vcc
	v_cmp_ge_i32_e32 vcc, v1, v65
	s_and_b32 s16, s16, 0x60
	s_lshl_b64 s[58:59], s[50:51], 16
	v_cndmask_b32_e64 v1, 0, 1, vcc
	v_cndmask_b32_e64 v1, v1, v20, s[6:7]
	v_and_b32_e32 v1, 1, v1
	v_cmp_eq_u32_e32 vcc, 1, v18
	v_or_b32_e32 v20, 3, v19
	s_and_b32 s61, s88, 7
	v_cndmask_b32_e32 v18, 0, v218, vcc
	v_cmp_eq_u32_e32 vcc, 1, v1
	s_mov_b32 s17, s41
	s_and_b32 s30, s30, 7
	v_cndmask_b32_e32 v1, 0, v219, vcc
	v_or_b32_e32 v18, v1, v18
	v_or_b32_e32 v1, 2, v19
	v_cmp_le_i32_e32 vcc, v1, v65
	s_lshl_b32 s44, s30, 10
	s_mov_b32 s45, s41
	v_cndmask_b32_e64 v21, 0, 1, vcc
	v_cmp_ge_i32_e32 vcc, v1, v65
	s_mov_b32 s47, s41
	s_xor_b32 s63, s61, 4
	v_cndmask_b32_e64 v22, 0, 1, vcc
	v_cmp_lt_i32_e32 vcc, v1, v65
	v_cndmask_b32_e64 v21, v22, v21, s[6:7]
	v_and_b32_e32 v21, 1, v21
	v_cndmask_b32_e64 v1, 0, 1, vcc
	v_cmp_ge_i32_e32 vcc, v20, v65
	s_mov_b32 s49, s41
	s_lshl_b32 s50, s63, 10
	v_cndmask_b32_e64 v20, 0, 1, vcc
	v_cndmask_b32_e64 v1, v20, v1, s[6:7]
	v_and_b32_e32 v1, 1, v1
	v_cmp_eq_u32_e32 vcc, 1, v21
	v_or_b32_e32 v21, 5, v19
	s_mov_b32 s51, s41
	v_cndmask_b32_e32 v20, 0, v218, vcc
	v_cmp_eq_u32_e32 vcc, 1, v1
	s_and_b32 s67, s37, 7
	s_and_b32 s66, s36, 7
	v_cndmask_b32_e32 v1, 0, v219, vcc
	v_or_b32_e32 v1, v1, v20
	v_or_b32_e32 v20, 4, v19
	v_cmp_le_i32_e32 vcc, v20, v65
	s_and_b32 s29, s29, 7
	s_lshl_b32 s52, s67, 10
	v_cndmask_b32_e64 v22, 0, 1, vcc
	v_cmp_ge_i32_e32 vcc, v20, v65
	s_mov_b32 s53, s41
	s_lshl_b32 s54, s66, 10
	v_cndmask_b32_e64 v23, 0, 1, vcc
	v_cmp_lt_i32_e32 vcc, v20, v65
	v_cndmask_b32_e64 v22, v23, v22, s[6:7]
	v_and_b32_e32 v22, 1, v22
	v_cndmask_b32_e64 v20, 0, 1, vcc
	v_cmp_ge_i32_e32 vcc, v21, v65
	s_mov_b32 s55, s41
	s_lshl_b32 s56, s29, 10
	v_cndmask_b32_e64 v21, 0, 1, vcc
	v_cndmask_b32_e64 v20, v21, v20, s[6:7]
	v_and_b32_e32 v20, 1, v20
	v_cmp_eq_u32_e32 vcc, 1, v22
	s_mov_b32 s57, s41
	s_mul_i32 s93, s33, 0x1200
	v_cndmask_b32_e32 v21, 0, v218, vcc
	v_cmp_eq_u32_e32 vcc, 1, v20
	v_add_u32_e32 v64, s93, v204
	v_mul_f32_e32 v98, 0, v184
	v_cndmask_b32_e32 v20, 0, v219, vcc
	v_or_b32_e32 v20, v20, v21
	v_or_b32_e32 v21, 6, v19
	v_cmp_le_i32_e32 vcc, v21, v65
	v_or_b32_e32 v19, 7, v19
	v_mov_b32_e32 v99, v98
	v_cndmask_b32_e64 v22, 0, 1, vcc
	v_cmp_ge_i32_e32 vcc, v21, v65
	v_mov_b32_e32 v100, v98
	v_mov_b32_e32 v101, v98
	v_cndmask_b32_e64 v23, 0, 1, vcc
	v_cmp_lt_i32_e32 vcc, v21, v65
	v_cndmask_b32_e64 v22, v23, v22, s[6:7]
	v_and_b32_e32 v22, 1, v22
	v_cndmask_b32_e64 v21, 0, 1, vcc
	v_cmp_ge_i32_e32 vcc, v19, v65
	v_add_u32_e32 v23, s16, v203
	s_lshl_b32 s16, s31, 5
	v_cndmask_b32_e64 v19, 0, 1, vcc
	v_cndmask_b32_e64 v19, v19, v21, s[6:7]
	v_and_b32_e32 v19, 1, v19
	v_cmp_eq_u32_e32 vcc, 1, v22
	s_and_b32 s16, s16, 0x60
	s_and_b32 s31, s31, 7
	v_cndmask_b32_e32 v21, 0, v218, vcc
	v_cmp_eq_u32_e32 vcc, 1, v19
	s_lshl_b32 s46, s31, 10
	s_mul_i32 s94, s60, 0x1200
	v_cndmask_b32_e32 v19, 0, v219, vcc
	v_cmp_le_i32_e32 vcc, v23, v65
	v_or_b32_e32 v19, v19, v21
	v_or_b32_e32 v21, 1, v23
	v_cndmask_b32_e64 v22, 0, 1, vcc
	v_cmp_ge_i32_e32 vcc, v23, v65
	v_add_u32_e32 v144, s94, v204
	s_mul_i32 s95, s62, 0x1200
	v_cndmask_b32_e64 v24, 0, 1, vcc
	v_cmp_lt_i32_e32 vcc, v23, v65
	v_cndmask_b32_e64 v22, v24, v22, s[6:7]
	v_and_b32_e32 v22, 1, v22
	v_cndmask_b32_e64 v24, 0, 1, vcc
	v_cmp_ge_i32_e32 vcc, v21, v65
	s_mulk_i32 s70, 0x1200
	s_lshl_b32 s96, s61, 6
	v_cndmask_b32_e64 v21, 0, 1, vcc
	v_cndmask_b32_e64 v21, v21, v24, s[6:7]
	v_and_b32_e32 v21, 1, v21
	v_cmp_eq_u32_e32 vcc, 1, v22
	v_or_b32_e32 v24, 3, v23
	s_lshl_b32 s97, s30, 6
	v_cndmask_b32_e32 v22, 0, v218, vcc
	v_cmp_eq_u32_e32 vcc, 1, v21
	s_lshl_b32 s36, s31, 6
	s_lshl_b32 s71, s63, 6
	v_cndmask_b32_e32 v21, 0, v219, vcc
	v_or_b32_e32 v22, v21, v22
	v_or_b32_e32 v21, 2, v23
	v_cmp_le_i32_e32 vcc, v21, v65
	s_lshl_b32 s72, s67, 6
	s_lshl_b32 s30, s66, 6
	v_cndmask_b32_e64 v25, 0, 1, vcc
	v_cmp_ge_i32_e32 vcc, v21, v65
	s_lshl_b32 s31, s29, 6
	s_mov_b32 s63, s41
	v_cndmask_b32_e64 v26, 0, 1, vcc
	v_cmp_lt_i32_e32 vcc, v21, v65
	v_cndmask_b32_e64 v25, v26, v25, s[6:7]
	v_and_b32_e32 v25, 1, v25
	v_cndmask_b32_e64 v21, 0, 1, vcc
	v_cmp_ge_i32_e32 vcc, v24, v65
	v_add_u32_e32 v223, 0x2000, v220
	v_add_u32_e32 v224, 0x4000, v220
	v_cndmask_b32_e64 v24, 0, 1, vcc
	v_cndmask_b32_e64 v21, v24, v21, s[6:7]
	v_and_b32_e32 v21, 1, v21
	v_cmp_eq_u32_e32 vcc, 1, v25
	v_or_b32_e32 v25, 5, v23
	v_add_u32_e32 v225, 0x6000, v220
	v_cndmask_b32_e32 v24, 0, v218, vcc
	v_cmp_eq_u32_e32 vcc, 1, v21
	v_mov_b32_e32 v192, v184
	v_mov_b32_e32 v193, v184
	v_cndmask_b32_e32 v21, 0, v219, vcc
	v_or_b32_e32 v21, v21, v24
	v_or_b32_e32 v24, 4, v23
	v_cmp_le_i32_e32 vcc, v24, v65
	v_mov_b32_e32 v191, v190
	v_mov_b32_e32 v194, v190
	v_cndmask_b32_e64 v26, 0, 1, vcc
	v_cmp_ge_i32_e32 vcc, v24, v65
	v_mov_b32_e32 v195, v190
	v_mov_b32_e32 v189, v188
	v_cndmask_b32_e64 v27, 0, 1, vcc
	v_cmp_lt_i32_e32 vcc, v24, v65
	v_cndmask_b32_e64 v26, v27, v26, s[6:7]
	v_and_b32_e32 v26, 1, v26
	v_cndmask_b32_e64 v24, 0, 1, vcc
	v_cmp_ge_i32_e32 vcc, v25, v65
	v_mov_b32_e32 v196, v188
	v_mov_b32_e32 v197, v188
	v_cndmask_b32_e64 v25, 0, 1, vcc
	v_cndmask_b32_e64 v24, v25, v24, s[6:7]
	v_and_b32_e32 v24, 1, v24
	v_cmp_eq_u32_e32 vcc, 1, v26
	s_mov_b32 s92, 2
	v_lshl_add_u64 v[198:199], s[64:65], 0, v[172:173]
	v_cndmask_b32_e32 v25, 0, v218, vcc
	v_cmp_eq_u32_e32 vcc, 1, v24
	s_nop 1
	v_cndmask_b32_e32 v24, 0, v219, vcc
	v_or_b32_e32 v24, v24, v25
	v_or_b32_e32 v25, 6, v23
	v_cmp_le_i32_e32 vcc, v25, v65
	v_or_b32_e32 v23, 7, v23
	s_nop 0
	v_cndmask_b32_e64 v26, 0, 1, vcc
	v_cmp_ge_i32_e32 vcc, v25, v65
	s_nop 1
	v_cndmask_b32_e64 v27, 0, 1, vcc
	v_cmp_lt_i32_e32 vcc, v25, v65
	v_cndmask_b32_e64 v26, v27, v26, s[6:7]
	v_and_b32_e32 v26, 1, v26
	v_cndmask_b32_e64 v25, 0, 1, vcc
	v_cmp_ge_i32_e32 vcc, v23, v65
	v_add_u32_e32 v27, s16, v203
	s_lshl_b32 s16, s28, 5
	v_cndmask_b32_e64 v23, 0, 1, vcc
	v_cndmask_b32_e64 v23, v23, v25, s[6:7]
	v_and_b32_e32 v23, 1, v23
	v_cmp_eq_u32_e32 vcc, 1, v26
	s_and_b32 s16, s16, 0x60
	s_and_b32 s28, s28, 7
	v_cndmask_b32_e32 v25, 0, v218, vcc
	v_cmp_eq_u32_e32 vcc, 1, v23
	s_lshl_b32 s48, s28, 10
	s_lshl_b32 s37, s28, 6
	v_cndmask_b32_e32 v23, 0, v219, vcc
	v_cmp_le_i32_e32 vcc, v27, v65
	v_or_b32_e32 v23, v23, v25
	v_or_b32_e32 v25, 1, v27
	v_cndmask_b32_e64 v26, 0, 1, vcc
	v_cmp_ge_i32_e32 vcc, v27, v65
	s_nop 1
	v_cndmask_b32_e64 v28, 0, 1, vcc
	v_cmp_lt_i32_e32 vcc, v27, v65
	v_cndmask_b32_e64 v26, v28, v26, s[6:7]
	v_and_b32_e32 v26, 1, v26
	v_cndmask_b32_e64 v28, 0, 1, vcc
	v_cmp_ge_i32_e32 vcc, v25, v65
	s_nop 1
	v_cndmask_b32_e64 v25, 0, 1, vcc
	v_cndmask_b32_e64 v25, v25, v28, s[6:7]
	v_and_b32_e32 v25, 1, v25
	v_cmp_eq_u32_e32 vcc, 1, v26
	v_or_b32_e32 v28, 3, v27
	s_nop 0
	v_cndmask_b32_e32 v26, 0, v218, vcc
	v_cmp_eq_u32_e32 vcc, 1, v25
	s_nop 1
	v_cndmask_b32_e32 v25, 0, v219, vcc
	v_or_b32_e32 v26, v25, v26
	v_or_b32_e32 v25, 2, v27
	v_cmp_le_i32_e32 vcc, v25, v65
	s_nop 1
	v_cndmask_b32_e64 v29, 0, 1, vcc
	v_cmp_ge_i32_e32 vcc, v25, v65
	s_nop 1
	v_cndmask_b32_e64 v30, 0, 1, vcc
	v_cmp_lt_i32_e32 vcc, v25, v65
	v_cndmask_b32_e64 v29, v30, v29, s[6:7]
	v_and_b32_e32 v29, 1, v29
	v_cndmask_b32_e64 v25, 0, 1, vcc
	v_cmp_ge_i32_e32 vcc, v28, v65
	s_nop 1
	v_cndmask_b32_e64 v28, 0, 1, vcc
	v_cndmask_b32_e64 v25, v28, v25, s[6:7]
	v_and_b32_e32 v25, 1, v25
	v_cmp_eq_u32_e32 vcc, 1, v29
	v_or_b32_e32 v29, 5, v27
	s_nop 0
	v_cndmask_b32_e32 v28, 0, v218, vcc
	v_cmp_eq_u32_e32 vcc, 1, v25
	s_nop 1
	v_cndmask_b32_e32 v25, 0, v219, vcc
	v_or_b32_e32 v25, v25, v28
	v_or_b32_e32 v28, 4, v27
	v_cmp_le_i32_e32 vcc, v28, v65
	s_nop 1
	v_cndmask_b32_e64 v30, 0, 1, vcc
	v_cmp_ge_i32_e32 vcc, v28, v65
	s_nop 1
	v_cndmask_b32_e64 v31, 0, 1, vcc
	v_cmp_lt_i32_e32 vcc, v28, v65
	v_cndmask_b32_e64 v30, v31, v30, s[6:7]
	v_and_b32_e32 v30, 1, v30
	v_cndmask_b32_e64 v28, 0, 1, vcc
	v_cmp_ge_i32_e32 vcc, v29, v65
	s_nop 1
	v_cndmask_b32_e64 v29, 0, 1, vcc
	v_cndmask_b32_e64 v28, v29, v28, s[6:7]
	v_and_b32_e32 v28, 1, v28
	v_cmp_eq_u32_e32 vcc, 1, v30
	s_nop 1
	v_cndmask_b32_e32 v29, 0, v218, vcc
	v_cmp_eq_u32_e32 vcc, 1, v28
	s_nop 1
	v_cndmask_b32_e32 v28, 0, v219, vcc
	v_or_b32_e32 v28, v28, v29
	v_or_b32_e32 v29, 6, v27
	v_cmp_le_i32_e32 vcc, v29, v65
	v_or_b32_e32 v27, 7, v27
	s_nop 0
	v_cndmask_b32_e64 v30, 0, 1, vcc
	v_cmp_ge_i32_e32 vcc, v29, v65
	s_nop 1
	v_cndmask_b32_e64 v31, 0, 1, vcc
	v_cmp_lt_i32_e32 vcc, v29, v65
	v_cndmask_b32_e64 v30, v31, v30, s[6:7]
	v_and_b32_e32 v30, 1, v30
	v_cndmask_b32_e64 v29, 0, 1, vcc
	v_cmp_ge_i32_e32 vcc, v27, v65
	v_add_u32_e32 v31, s16, v203
	s_lshl_b32 s16, s61, 10
	v_cndmask_b32_e64 v27, 0, 1, vcc
	v_cndmask_b32_e64 v27, v27, v29, s[6:7]
	v_and_b32_e32 v27, 1, v27
	v_cmp_eq_u32_e32 vcc, 1, v30
	v_or_b32_e32 v146, 5, v31
	s_add_u32 s28, s18, s58
	v_cndmask_b32_e32 v29, 0, v218, vcc
	v_cmp_eq_u32_e32 vcc, 1, v27
	s_addc_u32 s29, s19, s59
	v_lshl_add_u64 v[158:159], s[28:29], 0, v[174:175]
	v_cndmask_b32_e32 v27, 0, v219, vcc
	v_cmp_le_i32_e32 vcc, v31, v65
	v_or_b32_e32 v27, v27, v29
	v_or_b32_e32 v29, 1, v31
	v_cndmask_b32_e64 v30, 0, 1, vcc
	v_cmp_ge_i32_e32 vcc, v31, v65
	v_lshl_add_u64 v[160:161], v[158:159], 0, s[42:43]
	s_lshl_b32 s60, s60, 10
	v_cndmask_b32_e64 v32, 0, 1, vcc
	v_cmp_lt_i32_e32 vcc, v31, v65
	v_cndmask_b32_e64 v30, v32, v30, s[6:7]
	v_and_b32_e32 v30, 1, v30
	v_cndmask_b32_e64 v32, 0, 1, vcc
	v_cmp_ge_i32_e32 vcc, v29, v65
	s_mov_b32 s61, s41
	s_lshl_b32 s62, s62, 10
	v_cndmask_b32_e64 v29, 0, 1, vcc
	v_cndmask_b32_e64 v29, v29, v32, s[6:7]
	v_and_b32_e32 v29, 1, v29
	v_cmp_eq_u32_e32 vcc, 1, v30
	v_lshl_add_u64 v[32:33], v[182:183], 0, s[58:59]
	v_lshl_add_u64 v[34:35], v[32:33], 0, s[16:17]
	v_cndmask_b32_e32 v30, 0, v218, vcc
	v_cmp_eq_u32_e32 vcc, 1, v29
	v_lshl_add_u64 v[36:37], v[32:33], 0, s[44:45]
	global_load_dwordx4 v[60:63], v[34:35], off
	global_load_dwordx4 v[52:55], v[36:37], off
	v_cndmask_b32_e32 v29, 0, v219, vcc
	v_or_b32_e32 v30, v29, v30
	v_or_b32_e32 v29, 2, v31
	v_lshl_add_u64 v[34:35], v[32:33], 0, s[46:47]
	v_lshl_add_u64 v[36:37], v[32:33], 0, s[48:49]
	global_load_dwordx4 v[56:59], v[34:35], off
	global_load_dwordx4 v[44:47], v[36:37], off
	v_lshl_add_u64 v[34:35], v[32:33], 0, s[50:51]
	v_cmp_le_i32_e32 vcc, v29, v65
	v_lshl_add_u64 v[36:37], v[32:33], 0, s[52:53]
	global_load_dwordx4 v[48:51], v[34:35], off
	global_load_dwordx4 v[40:43], v[36:37], off
	v_lshl_add_u64 v[34:35], v[32:33], 0, s[54:55]
	v_lshl_add_u64 v[32:33], v[32:33], 0, s[56:57]
	v_cndmask_b32_e64 v122, 0, 1, vcc
	v_cmp_ge_i32_e32 vcc, v29, v65
	global_load_dwordx4 v[36:39], v[34:35], off
	s_nop 0
	global_load_dwordx4 v[32:35], v[32:33], off
	s_barrier
	ds_read_b64_tr_b16 v[104:105], v64 offset:34368
	ds_read_b64_tr_b16 v[102:103], v64 offset:33792
	ds_read_b64_tr_b16 v[106:107], v64 offset:33824
	ds_read_b64_tr_b16 v[110:111], v64 offset:33856
	ds_read_b64_tr_b16 v[114:115], v64 offset:33888
	ds_read_b64_tr_b16 v[108:109], v64 offset:34400
	ds_read_b64_tr_b16 v[112:113], v64 offset:34432
	ds_read_b64_tr_b16 v[116:117], v64 offset:34464
	v_or_b32_e32 v64, 3, v31
	v_cndmask_b32_e64 v123, 0, 1, vcc
	v_cmp_lt_i32_e32 vcc, v29, v65
	v_cndmask_b32_e64 v126, v123, v122, s[6:7]
	v_and_b32_e32 v138, 1, v126
	v_cndmask_b32_e64 v29, 0, 1, vcc
	v_cmp_ge_i32_e32 vcc, v64, v65
	s_waitcnt vmcnt(17) lgkmcnt(6)
	v_mfma_f32_16x16x32_bf16 v[118:121], v[90:93], v[102:105], v[98:101]
	s_lshl_b32 s58, s33, 10
	v_cndmask_b32_e64 v64, 0, 1, vcc
	v_cndmask_b32_e64 v29, v64, v29, s[6:7]
	v_and_b32_e32 v29, 1, v29
	v_cmp_eq_u32_e32 vcc, 1, v138
	s_waitcnt vmcnt(13)
	v_mfma_f32_16x16x32_bf16 v[102:105], v[94:97], v[102:105], v[98:101]
	s_mov_b32 s59, s41
	v_cndmask_b32_e32 v64, 0, v218, vcc
	v_cmp_eq_u32_e32 vcc, 1, v29
	s_waitcnt lgkmcnt(2)
	v_mfma_f32_16x16x32_bf16 v[122:125], v[90:93], v[106:109], v[98:101]
	s_mov_b32 s33, 34
	v_cndmask_b32_e32 v29, 0, v219, vcc
	v_or_b32_e32 v29, v29, v64
	v_or_b32_e32 v64, 4, v31
	v_cmp_le_i32_e32 vcc, v64, v65
	v_mfma_f32_16x16x32_bf16 v[106:109], v[94:97], v[106:109], v[98:101]
	s_nop 0
	v_cndmask_b32_e64 v147, 0, 1, vcc
	v_cmp_ge_i32_e32 vcc, v64, v65
	s_waitcnt lgkmcnt(1)
	v_mfma_f32_16x16x32_bf16 v[126:129], v[90:93], v[110:113], v[98:101]
	v_cndmask_b32_e64 v148, 0, 1, vcc
	v_cmp_lt_i32_e32 vcc, v64, v65
	v_mfma_f32_16x16x32_bf16 v[110:113], v[94:97], v[110:113], v[98:101]
	v_cndmask_b32_e64 v147, v148, v147, s[6:7]
	v_cndmask_b32_e64 v64, 0, 1, vcc
	v_cmp_ge_i32_e32 vcc, v146, v65
	s_waitcnt lgkmcnt(0)
	v_mfma_f32_16x16x32_bf16 v[90:93], v[90:93], v[114:117], v[98:101]
	v_and_b32_e32 v147, 1, v147
	v_or_b32_e32 v146, 6, v31
	v_or_b32_e32 v31, 7, v31
	v_mfma_f32_16x16x32_bf16 v[94:97], v[94:97], v[114:117], v[98:101]
	s_nop 2
	ds_read_b64_tr_b16 v[100:101], v144 offset:34368
	ds_read_b64_tr_b16 v[98:99], v144 offset:33792
	ds_read_b64_tr_b16 v[114:115], v144 offset:33824
	ds_read_b64_tr_b16 v[138:139], v144 offset:33856
	ds_read_b64_tr_b16 v[142:143], v144 offset:33888
	ds_read_b64_tr_b16 v[116:117], v144 offset:34400
	ds_read_b64_tr_b16 v[140:141], v144 offset:34432
	ds_read_b64_tr_b16 v[144:145], v144 offset:34464
	s_waitcnt lgkmcnt(6)
	v_mfma_f32_16x16x32_bf16 v[118:121], v[82:85], v[98:101], v[118:121]
	s_waitcnt vmcnt(12)
	v_mfma_f32_16x16x32_bf16 v[98:101], v[86:89], v[98:101], v[102:105]
	s_waitcnt lgkmcnt(2)
	v_mfma_f32_16x16x32_bf16 v[102:105], v[82:85], v[114:117], v[122:125]
	s_nop 2
	v_cndmask_b32_e64 v122, 0, 1, vcc
	v_cndmask_b32_e64 v64, v122, v64, s[6:7]
	v_and_b32_e32 v64, 1, v64
	v_cmp_eq_u32_e32 vcc, 1, v147
	v_mfma_f32_16x16x32_bf16 v[106:109], v[86:89], v[114:117], v[106:109]
	s_nop 0
	v_cndmask_b32_e32 v122, 0, v218, vcc
	v_cmp_eq_u32_e32 vcc, 1, v64
	s_waitcnt lgkmcnt(1)
	v_mfma_f32_16x16x32_bf16 v[114:117], v[82:85], v[138:141], v[126:129]
	v_cndmask_b32_e32 v64, 0, v219, vcc
	v_cmp_le_i32_e32 vcc, v146, v65
	v_or_b32_e32 v64, v64, v122
	s_waitcnt lgkmcnt(0)
	v_mfma_f32_16x16x32_bf16 v[82:85], v[82:85], v[142:145], v[90:93]
	v_cndmask_b32_e64 v122, 0, 1, vcc
	v_cmp_ge_i32_e32 vcc, v146, v65
	v_add_u32_e32 v128, s95, v204
	v_mfma_f32_16x16x32_bf16 v[110:113], v[86:89], v[138:141], v[110:113]
	v_cndmask_b32_e64 v90, 0, 1, vcc
	v_cndmask_b32_e64 v138, v90, v122, s[6:7]
	v_cmp_lt_i32_e32 vcc, v146, v65
	v_mfma_f32_16x16x32_bf16 v[86:89], v[86:89], v[142:145], v[94:97]
	ds_read_b64_tr_b16 v[92:93], v128 offset:34368
	ds_read_b64_tr_b16 v[90:91], v128 offset:33792
	s_nop 0
	ds_read_b64_tr_b16 v[94:95], v128 offset:33824
	ds_read_b64_tr_b16 v[122:123], v128 offset:33856
	ds_read_b64_tr_b16 v[126:127], v128 offset:33888
	ds_read_b64_tr_b16 v[96:97], v128 offset:34400
	ds_read_b64_tr_b16 v[124:125], v128 offset:34432
	ds_read_b64_tr_b16 v[128:129], v128 offset:34464
	v_and_b32_e32 v142, 1, v138
	v_cndmask_b32_e64 v138, 0, 1, vcc
	v_cmp_ge_i32_e32 vcc, v31, v65
	s_waitcnt vmcnt(11) lgkmcnt(0)
	v_mfma_f32_16x16x32_bf16 v[150:153], v[78:81], v[126:129], v[86:89]
	v_cndmask_b32_e64 v31, 0, 1, vcc
	v_cndmask_b32_e64 v31, v31, v138, s[6:7]
	s_nop 0
	v_add_u32_e32 v86, s70, v204
	v_mfma_f32_16x16x32_bf16 v[118:121], v[74:77], v[90:93], v[118:121]
	v_cmp_eq_u32_e32 vcc, 1, v142
	v_and_b32_e32 v31, 1, v31
	v_mfma_f32_16x16x32_bf16 v[90:93], v[78:81], v[90:93], v[98:101]
	v_mfma_f32_16x16x32_bf16 v[138:141], v[74:77], v[94:97], v[102:105]
	s_nop 1
	v_cndmask_b32_e32 v98, 0, v218, vcc
	v_cmp_eq_u32_e32 vcc, 1, v31
	v_mfma_f32_16x16x32_bf16 v[142:145], v[78:81], v[94:97], v[106:109]
	s_nop 0
	v_cndmask_b32_e32 v31, 0, v219, vcc
	v_or_b32_e32 v31, v31, v98
	v_mfma_f32_16x16x32_bf16 v[146:149], v[74:77], v[122:125], v[114:117]
	v_mfma_f32_16x16x32_bf16 v[122:125], v[78:81], v[122:125], v[110:113]
	v_mfma_f32_16x16x32_bf16 v[74:77], v[74:77], v[126:129], v[82:85]
	ds_read_b64_tr_b16 v[80:81], v86 offset:34368
	ds_read_b64_tr_b16 v[78:79], v86 offset:33792
	s_nop 0
	ds_read_b64_tr_b16 v[82:83], v86 offset:33824
	ds_read_b64_tr_b16 v[126:127], v86 offset:33856
	ds_read_b64_tr_b16 v[154:155], v86 offset:33888
	ds_read_b64_tr_b16 v[84:85], v86 offset:34400
	ds_read_b64_tr_b16 v[128:129], v86 offset:34432
	ds_read_b64_tr_b16 v[156:157], v86 offset:34464
	s_waitcnt lgkmcnt(6)
	v_mfma_f32_16x16x32_bf16 v[98:101], v[66:69], v[78:81], v[118:121]
	s_waitcnt vmcnt(10)
	v_mfma_f32_16x16x32_bf16 v[102:105], v[70:73], v[78:81], v[90:93]
	v_lshl_add_u64 v[78:79], v[158:159], 0, s[58:59]
	v_lshl_add_u64 v[80:81], v[160:161], 0, s[58:59]
	global_load_dwordx4 v[94:97], v[78:79], off
	global_load_dwordx4 v[90:93], v[80:81], off
	s_waitcnt lgkmcnt(2)
	v_mfma_f32_16x16x32_bf16 v[106:109], v[66:69], v[82:85], v[138:141]
	v_lshl_add_u64 v[78:79], v[158:159], 0, s[60:61]
	v_lshl_add_u64 v[80:81], v[160:161], 0, s[60:61]
	global_load_dwordx4 v[86:89], v[78:79], off
	s_nop 0
	global_load_dwordx4 v[78:81], v[80:81], off
	v_mfma_f32_16x16x32_bf16 v[114:117], v[70:73], v[82:85], v[142:145]
	v_lshl_add_u64 v[82:83], v[158:159], 0, s[62:63]
	s_waitcnt lgkmcnt(1)
	v_mfma_f32_16x16x32_bf16 v[110:113], v[66:69], v[126:129], v[146:149]
	v_mfma_f32_16x16x32_bf16 v[126:129], v[70:73], v[126:129], v[122:125]
	v_cvt_pk_bf16_f32 v138, v98, v99
	s_waitcnt lgkmcnt(0)
	v_mfma_f32_16x16x32_bf16 v[122:125], v[66:69], v[154:157], v[74:77]
	v_lshl_add_u64 v[66:67], v[160:161], 0, s[62:63]
	global_load_dwordx4 v[82:85], v[82:83], off
	s_nop 0
	global_load_dwordx4 v[74:77], v[66:67], off
	v_lshl_add_u64 v[66:67], v[158:159], 0, s[40:41]
	v_lshl_add_u64 v[68:69], v[160:161], 0, s[40:41]
	v_mfma_f32_16x16x32_bf16 v[118:121], v[70:73], v[154:157], v[150:153]
	global_load_dwordx4 v[70:73], v[66:67], off
	s_nop 0
	global_load_dwordx4 v[66:69], v[68:69], off
	v_cvt_pk_bf16_f32 v139, v100, v101
	v_cvt_pk_bf16_f32 v140, v106, v107
	v_cvt_pk_bf16_f32 v141, v108, v109
	v_cvt_pk_bf16_f32 v142, v110, v111
	v_cvt_pk_bf16_f32 v143, v112, v113
	v_cvt_pk_bf16_f32 v144, v122, v123
	v_cvt_pk_bf16_f32 v145, v124, v125
	v_cvt_pk_bf16_f32 v146, v102, v103
	v_cvt_pk_bf16_f32 v147, v104, v105
	ds_write2_b64 v220, v[138:139], v[146:147] offset1:4
	v_cvt_pk_bf16_f32 v138, v114, v115
	v_cvt_pk_bf16_f32 v139, v116, v117
	ds_write2_b64 v223, v[140:141], v[138:139] offset0:32 offset1:36
	v_cvt_pk_bf16_f32 v138, v126, v127
	v_cvt_pk_bf16_f32 v139, v128, v129
	ds_write2_b64 v224, v[142:143], v[138:139] offset0:64 offset1:68
	v_cvt_pk_bf16_f32 v138, v118, v119
	v_cvt_pk_bf16_f32 v139, v120, v121
	ds_write2_b64 v225, v[144:145], v[138:139] offset0:96 offset1:100
	s_waitcnt vmcnt(17)
	v_lshlrev_b32_e32 v138, 16, v134
	v_and_b32_e32 v134, 0xffff0000, v134
	v_mul_f32_e32 v138, v221, v138
	v_mul_f32_e32 v134, v221, v134
	v_cvt_pk_bf16_f32 v134, v138, v134
	v_lshlrev_b32_e32 v138, 16, v135
	v_and_b32_e32 v135, 0xffff0000, v135
	v_mul_f32_e32 v138, v221, v138
	v_mul_f32_e32 v135, v221, v135
	v_cvt_pk_bf16_f32 v135, v138, v135
	v_lshlrev_b32_e32 v138, 16, v136
	v_and_b32_e32 v136, 0xffff0000, v136
	v_mul_f32_e32 v138, v221, v138
	v_mul_f32_e32 v136, v221, v136
	v_cvt_pk_bf16_f32 v136, v138, v136
	v_lshlrev_b32_e32 v138, 16, v137
	v_and_b32_e32 v137, 0xffff0000, v137
	v_mul_f32_e32 v137, v221, v137
	v_mul_f32_e32 v138, v221, v138
	v_cvt_pk_bf16_f32 v137, v138, v137
	ds_write_b128 v209, v[134:137] offset:52224
	s_waitcnt vmcnt(16)
	v_lshlrev_b32_e32 v134, 16, v130
	v_and_b32_e32 v130, 0xffff0000, v130
	v_mul_f32_e32 v134, v222, v134
	v_mul_f32_e32 v130, v222, v130
	v_cvt_pk_bf16_f32 v130, v134, v130
	v_lshlrev_b32_e32 v134, 16, v131
	v_and_b32_e32 v131, 0xffff0000, v131
	v_mul_f32_e32 v134, v222, v134
	v_mul_f32_e32 v131, v222, v131
	v_cvt_pk_bf16_f32 v131, v134, v131
	v_lshlrev_b32_e32 v134, 16, v132
	v_and_b32_e32 v132, 0xffff0000, v132
	v_mul_f32_e32 v134, v222, v134
	v_mul_f32_e32 v132, v222, v132
	v_cvt_pk_bf16_f32 v132, v134, v132
	v_lshlrev_b32_e32 v134, 16, v133
	v_and_b32_e32 v133, 0xffff0000, v133
	v_mul_f32_e32 v133, v222, v133
	v_mul_f32_e32 v134, v222, v134
	v_cvt_pk_bf16_f32 v133, v134, v133
	ds_write_b128 v209, v[130:133] offset:61440
	s_waitcnt lgkmcnt(0)
	s_barrier
	s_branch .LBB0_2524

.LBB0_2534:
	s_waitcnt lgkmcnt(0)
	s_barrier
	ds_read_b64_tr_b16 v[140:141], v226 offset:34368
	ds_read_b64_tr_b16 v[138:139], v226 offset:33792
	v_mov_b32_e32 v185, v184
	v_pk_mul_f32 v[100:101], v[184:185], v[100:101]
	v_pk_mul_f32 v[98:99], v[192:193], v[98:99]
	v_pk_mul_f32 v[104:105], v[184:185], v[104:105]
	v_pk_mul_f32 v[102:103], v[192:193], v[102:103]
	s_waitcnt vmcnt(17) lgkmcnt(0)
	v_mfma_f32_16x16x32_bf16 v[98:101], v[94:97], v[138:141], v[98:101]
	ds_read_b64_tr_b16 v[142:143], v226 offset:33824
	ds_read_b64_tr_b16 v[144:145], v226 offset:34400
	v_pk_mul_f32 v[112:113], v[184:185], v[112:113]
	s_waitcnt vmcnt(16)
	v_mfma_f32_16x16x32_bf16 v[102:105], v[90:93], v[138:141], v[102:105]
	ds_read_b64_tr_b16 v[138:139], v226 offset:33856
	ds_read_b64_tr_b16 v[140:141], v226 offset:34432
	v_pk_mul_f32 v[110:111], v[192:193], v[110:111]
	v_pk_mul_f32 v[128:129], v[184:185], v[128:129]
	v_pk_mul_f32 v[126:127], v[192:193], v[126:127]
	s_waitcnt lgkmcnt(0)
	v_mfma_f32_16x16x32_bf16 v[110:113], v[94:97], v[138:141], v[110:113]
	v_mul_f32_e64 v108, v184, v108
	v_mul_f32_e64 v109, v185, v109
	v_pk_mul_f32 v[106:107], v[192:193], v[106:107]
	v_pk_mul_f32 v[116:117], v[184:185], v[116:117]
	v_mfma_f32_16x16x32_bf16 v[126:129], v[90:93], v[138:141], v[126:129]
	ds_read_b64_tr_b16 v[138:139], v226 offset:33888
	ds_read_b64_tr_b16 v[140:141], v226 offset:34464
	v_pk_mul_f32 v[114:115], v[192:193], v[114:115]
	v_pk_mul_f32 v[124:125], v[184:185], v[124:125]
	v_pk_mul_f32 v[122:123], v[192:193], v[122:123]
	v_pk_mul_f32 v[120:121], v[184:185], v[120:121]
	v_pk_mul_f32 v[118:119], v[192:193], v[118:119]
	v_mfma_f32_16x16x32_bf16 v[106:109], v[94:97], v[142:145], v[106:109]
	s_add_u32 s28, s18, s68
	s_addc_u32 s29, s19, s69
	v_lshl_add_u64 v[146:147], s[28:29], 0, v[174:175]
	v_mfma_f32_16x16x32_bf16 v[114:117], v[90:93], v[142:145], v[114:117]
	v_lshl_add_u64 v[148:149], v[146:147], 0, s[42:43]
	s_andn2_b64 vcc, exec, s[66:67]
	s_waitcnt lgkmcnt(0)
	v_mfma_f32_16x16x32_bf16 v[94:97], v[94:97], v[138:141], v[122:125]
	v_mfma_f32_16x16x32_bf16 v[90:93], v[90:93], v[138:141], v[118:121]
	s_nop 2
	ds_read_b64_tr_b16 v[120:121], v227 offset:34368
	ds_read_b64_tr_b16 v[118:119], v227 offset:33792
	ds_read_b64_tr_b16 v[122:123], v227 offset:33824
	ds_read_b64_tr_b16 v[124:125], v227 offset:34400
	s_waitcnt vmcnt(15) lgkmcnt(2)
	v_mfma_f32_16x16x32_bf16 v[98:101], v[86:89], v[118:121], v[98:101]
	s_waitcnt vmcnt(14)
	v_mfma_f32_16x16x32_bf16 v[102:105], v[78:81], v[118:121], v[102:105]
	ds_read_b64_tr_b16 v[118:119], v227 offset:33856
	ds_read_b64_tr_b16 v[120:121], v227 offset:34432
	s_waitcnt lgkmcnt(2)
	v_mfma_f32_16x16x32_bf16 v[106:109], v[86:89], v[122:125], v[106:109]
	v_mfma_f32_16x16x32_bf16 v[114:117], v[78:81], v[122:125], v[114:117]
	ds_read_b64_tr_b16 v[124:125], v227 offset:34464
	ds_read_b64_tr_b16 v[122:123], v227 offset:33888
	s_waitcnt lgkmcnt(2)
	v_mfma_f32_16x16x32_bf16 v[110:113], v[86:89], v[118:121], v[110:113]
	v_mfma_f32_16x16x32_bf16 v[118:121], v[78:81], v[118:121], v[126:129]
	s_waitcnt lgkmcnt(0)
	v_mfma_f32_16x16x32_bf16 v[86:89], v[86:89], v[122:125], v[94:97]
	s_nop 2
	ds_read_b64_tr_b16 v[94:95], v228 offset:34368
	v_mfma_f32_16x16x32_bf16 v[78:81], v[78:81], v[122:125], v[90:93]
	ds_read_b64_tr_b16 v[122:123], v228 offset:33856
	ds_read_b64_tr_b16 v[124:125], v228 offset:34432
	s_nop 0
	ds_read_b64_tr_b16 v[92:93], v228 offset:33792
	ds_read_b64_tr_b16 v[90:91], v228 offset:33824
	s_waitcnt vmcnt(12) lgkmcnt(1)
	v_mfma_f32_16x16x32_bf16 v[96:99], v[82:85], v[92:95], v[98:101]
	s_waitcnt vmcnt(11)
	v_mfma_f32_16x16x32_bf16 v[102:105], v[74:77], v[92:95], v[102:105]
	ds_read_b64_tr_b16 v[92:93], v228 offset:34400
	s_waitcnt lgkmcnt(0)
	v_mfma_f32_16x16x32_bf16 v[106:109], v[82:85], v[90:93], v[106:109]
	v_mfma_f32_16x16x32_bf16 v[114:117], v[74:77], v[90:93], v[114:117]
	ds_read_b64_tr_b16 v[92:93], v228 offset:34464
	ds_read_b64_tr_b16 v[90:91], v228 offset:33888
	v_mfma_f32_16x16x32_bf16 v[110:113], v[82:85], v[122:125], v[110:113]
	v_mfma_f32_16x16x32_bf16 v[118:121], v[74:77], v[122:125], v[118:121]
	s_waitcnt lgkmcnt(0)
	v_mfma_f32_16x16x32_bf16 v[122:125], v[82:85], v[90:93], v[86:89]
	ds_read_b64_tr_b16 v[84:85], v229 offset:34368
	ds_read_b64_tr_b16 v[82:83], v229 offset:33792
	v_mfma_f32_16x16x32_bf16 v[138:141], v[74:77], v[90:93], v[78:81]
	ds_read_b64_tr_b16 v[74:75], v229 offset:33824
	ds_read_b64_tr_b16 v[76:77], v229 offset:34400
	s_nop 0
	v_lshl_add_u64 v[78:79], v[146:147], 0, s[58:59]
	s_waitcnt vmcnt(11) lgkmcnt(2)
	v_mfma_f32_16x16x32_bf16 v[98:101], v[70:73], v[82:85], v[96:99]
	s_nop 2
	global_load_dwordx4 v[94:97], v[78:79], off
	v_lshl_add_u64 v[78:79], v[148:149], 0, s[58:59]
	global_load_dwordx4 v[90:93], v[78:79], off
	s_waitcnt lgkmcnt(0)
	v_mfma_f32_16x16x32_bf16 v[106:109], v[70:73], v[74:77], v[106:109]
	v_lshl_add_u64 v[78:79], v[146:147], 0, s[60:61]
	s_waitcnt vmcnt(12)
	v_mfma_f32_16x16x32_bf16 v[114:117], v[66:69], v[74:77], v[114:117]
	v_lshl_add_u64 v[74:75], v[148:149], 0, s[60:61]
	v_mfma_f32_16x16x32_bf16 v[102:105], v[66:69], v[82:85], v[102:105]
	ds_read_b64_tr_b16 v[82:83], v229 offset:33856
	ds_read_b64_tr_b16 v[84:85], v229 offset:34432
	global_load_dwordx4 v[86:89], v[78:79], off
	s_nop 0
	global_load_dwordx4 v[78:81], v[74:75], off
	ds_read_b64_tr_b16 v[142:143], v229 offset:33888
	ds_read_b64_tr_b16 v[144:145], v229 offset:34464
	s_waitcnt lgkmcnt(2)
	v_mfma_f32_16x16x32_bf16 v[110:113], v[70:73], v[82:85], v[110:113]
	v_lshl_add_u64 v[74:75], v[146:147], 0, s[62:63]
	s_waitcnt lgkmcnt(0)
	v_mfma_f32_16x16x32_bf16 v[122:125], v[70:73], v[142:145], v[122:125]
	v_lshl_add_u64 v[70:71], v[146:147], 0, s[40:41]
	global_load_dwordx4 v[70:73], v[70:71], off
	v_lshl_add_u64 v[146:147], v[148:149], 0, s[40:41]
	v_mfma_f32_16x16x32_bf16 v[126:129], v[66:69], v[82:85], v[118:121]
	global_load_dwordx4 v[82:85], v[74:75], off
	v_lshl_add_u64 v[74:75], v[148:149], 0, s[62:63]
	global_load_dwordx4 v[74:77], v[74:75], off
	v_mfma_f32_16x16x32_bf16 v[118:121], v[66:69], v[142:145], v[138:141]
	global_load_dwordx4 v[66:69], v[146:147], off
	v_cvt_pk_bf16_f32 v138, v98, v99
	v_cvt_pk_bf16_f32 v139, v100, v101
	v_cvt_pk_bf16_f32 v140, v106, v107
	v_cvt_pk_bf16_f32 v141, v108, v109
	v_cvt_pk_bf16_f32 v142, v110, v111
	v_cvt_pk_bf16_f32 v143, v112, v113
	v_cvt_pk_bf16_f32 v144, v122, v123
	v_cvt_pk_bf16_f32 v145, v124, v125
	v_cvt_pk_bf16_f32 v146, v102, v103
	v_cvt_pk_bf16_f32 v147, v104, v105
	ds_write2_b64 v220, v[138:139], v[146:147] offset1:4
	v_cvt_pk_bf16_f32 v138, v114, v115
	v_cvt_pk_bf16_f32 v139, v116, v117
	ds_write2_b64 v223, v[140:141], v[138:139] offset0:32 offset1:36
	v_cvt_pk_bf16_f32 v138, v126, v127
	v_cvt_pk_bf16_f32 v139, v128, v129
	ds_write2_b64 v224, v[142:143], v[138:139] offset0:64 offset1:68
	v_cvt_pk_bf16_f32 v138, v118, v119
	v_cvt_pk_bf16_f32 v139, v120, v121
	ds_write2_b64 v225, v[144:145], v[138:139] offset0:96 offset1:100
	s_cbranch_vccnz .LBB0_2523
	s_and_b64 s[28:29], s[64:65], exec
	s_cselect_b32 s64, 0, s33
	s_and_b64 s[28:29], s[6:7], exec
	s_cselect_b32 s28, s73, s64
	s_or_b32 s29, s28, s90
	s_add_i32 s64, s28, s91
	s_cmp_lt_u32 s28, 2
	s_cselect_b32 s28, s29, s64
	ds_read_b128 v[138:141], v210
	v_lshl_add_u32 v142, s28, 7, v205
	v_ashrrev_i32_e32 v143, 31, v142
	v_lshlrev_b64 v[142:143], 12, v[142:143]
	v_lshl_add_u64 v[142:143], v[198:199], 0, v[142:143]
	s_waitcnt lgkmcnt(0)
	global_store_dwordx4 v[142:143], v[138:141], off
	ds_read_b128 v[138:141], v210 offset:9216
	v_add_co_u32_e32 v142, vcc, 0x40000, v142
	s_nop 1
	v_addc_co_u32_e32 v143, vcc, 0, v143, vcc
	s_waitcnt lgkmcnt(0)
	global_store_dwordx4 v[142:143], v[138:141], off
	s_branch .LBB0_2523
